# bal_nops
# speedup vs baseline: 1.0045x; 1.0045x over previous
.LBB0_4:
	s_or_b64 exec, exec, s[4:5]
	s_waitcnt lgkmcnt(0)
	s_barrier
	ds_read_b32 v15, v14
	ds_add_rtn_u32 v14, v14, v3 offset:256
	s_load_dwordx2 s[4:5], s[0:1], 0x20
	s_waitcnt lgkmcnt(0)
	v_add_u32_e32 v14, v14, v15
	v_ashrrev_i32_e32 v16, 8, v14
	v_sub_u32_e32 v17, 15, v16
	v_cmp_gt_i32_e64 s[2:3], 8, v16
	v_lshrrev_b32_e32 v15, 6, v14
	s_nop 0
	v_cndmask_b32_e64 v16, v17, v16, s[2:3]
	v_cndmask_b32_e64 v17, 4, 0, s[2:3]
	v_mov_b32_e32 v20, 0x90
	v_lshrrev_b32_e32 v20, v16, v20
	v_and_b32_e32 v20, 1, v20
	v_mul_u32_u24_e32 v20, 3, v20
	v_xor_b32_e32 v16, v16, v20
	v_and_or_b32 v17, v15, 3, v17
	v_lshlrev_b32_e32 v15, 6, v16
	v_lshl_add_u32 v15, v17, 9, v15
	v_and_or_b32 v14, v14, 63, v15
	v_ashrrev_i32_e32 v15, 31, v14
	v_lshl_add_u64 v[14:15], v[14:15], 2, s[6:7]
	global_store_dword v[14:15], v0, off
	v_lshlrev_b32_e32 v14, 2, v17
	v_lshl_or_b32 v14, v16, 5, v14
	ds_max_i32 v14, v12 offset:768
	ds_read_b32 v12, v13
	ds_add_rtn_u32 v13, v13, v3 offset:256
	s_waitcnt lgkmcnt(0)
	v_add_u32_e32 v12, v13, v12
	v_ashrrev_i32_e32 v14, 8, v12
	v_sub_u32_e32 v15, 15, v14
	v_cmp_gt_i32_e64 s[2:3], 8, v14
	v_lshrrev_b32_e32 v13, 6, v12
	s_nop 0
	v_cndmask_b32_e64 v14, v15, v14, s[2:3]
	v_cndmask_b32_e64 v15, 4, 0, s[2:3]
	v_mov_b32_e32 v20, 0x90
	v_lshrrev_b32_e32 v20, v14, v20
	v_and_b32_e32 v20, 1, v20
	v_mul_u32_u24_e32 v20, 3, v20
	v_xor_b32_e32 v14, v14, v20
	v_and_or_b32 v15, v13, 3, v15
	v_lshlrev_b32_e32 v13, 6, v14
	v_lshl_add_u32 v13, v15, 9, v13
	v_and_or_b32 v12, v12, 63, v13
	v_ashrrev_i32_e32 v13, 31, v12
	v_lshl_add_u64 v[12:13], v[12:13], 2, s[6:7]
	global_store_dword v[12:13], v8, off
	v_lshlrev_b32_e32 v8, 2, v15
	v_lshl_or_b32 v8, v14, 5, v8
	ds_max_i32 v8, v10 offset:768
	ds_read_b32 v8, v11
	ds_add_rtn_u32 v10, v11, v3 offset:256
	s_waitcnt lgkmcnt(0)
	v_add_u32_e32 v8, v10, v8
	v_ashrrev_i32_e32 v11, 8, v8
	v_sub_u32_e32 v12, 15, v11
	v_cmp_gt_i32_e64 s[2:3], 8, v11
	v_lshrrev_b32_e32 v10, 6, v8
	s_nop 0
	v_cndmask_b32_e64 v12, v12, v11, s[2:3]
	v_cndmask_b32_e64 v11, 4, 0, s[2:3]
	v_mov_b32_e32 v20, 0x90
	v_lshrrev_b32_e32 v20, v12, v20
	v_and_b32_e32 v20, 1, v20
	v_mul_u32_u24_e32 v20, 3, v20
	v_xor_b32_e32 v12, v12, v20
	v_and_or_b32 v13, v10, 3, v11
	v_lshlrev_b32_e32 v10, 6, v12
	v_lshl_add_u32 v10, v13, 9, v10
	v_and_or_b32 v10, v8, 63, v10
	v_ashrrev_i32_e32 v11, 31, v10
	v_lshl_add_u64 v[10:11], v[10:11], 2, s[6:7]
	global_store_dword v[10:11], v6, off
	v_lshlrev_b32_e32 v6, 2, v13
	v_lshl_or_b32 v6, v12, 5, v6
	ds_max_i32 v6, v7 offset:768
	ds_read_b32 v6, v9
	ds_add_rtn_u32 v3, v9, v3 offset:256
	s_waitcnt lgkmcnt(0)
	v_add_u32_e32 v3, v3, v6
	v_ashrrev_i32_e32 v7, 8, v3
	v_sub_u32_e32 v8, 15, v7
	v_cmp_gt_i32_e64 s[2:3], 8, v7
	v_lshrrev_b32_e32 v6, 6, v3
	s_nop 0
	v_cndmask_b32_e64 v8, v8, v7, s[2:3]
	v_cndmask_b32_e64 v7, 4, 0, s[2:3]
	v_mov_b32_e32 v20, 0x90
	v_lshrrev_b32_e32 v20, v8, v20
	v_and_b32_e32 v20, 1, v20
	v_mul_u32_u24_e32 v20, 3, v20
	v_xor_b32_e32 v8, v8, v20
	v_and_or_b32 v9, v6, 3, v7
	v_lshlrev_b32_e32 v6, 6, v8
	v_lshl_add_u32 v6, v9, 9, v6
	v_and_or_b32 v6, v3, 63, v6
	v_ashrrev_i32_e32 v7, 31, v6
	v_lshl_add_u64 v[6:7], v[6:7], 2, s[6:7]
	v_lshlrev_b32_e32 v3, 2, v9
	global_store_dword v[6:7], v4, off
	v_lshl_or_b32 v3, v8, 5, v3
	ds_max_i32 v3, v5 offset:768
	s_waitcnt lgkmcnt(0)
	s_barrier
	s_and_saveexec_b64 s[6:7], vcc
	s_cbranch_execz .LBB0_14
	v_and_b32_e32 v3, 60, v0
	v_add_u32_e32 v5, 1, v0
	v_sub_u32_e32 v6, v5, v3
	v_cmp_lt_u32_e64 s[2:3], 1, v6
	s_mov_b64 s[10:11], -1
	v_mov_b32_e32 v4, 0
	s_and_saveexec_b64 s[8:9], s[2:3]
	s_cbranch_execz .LBB0_9
	v_and_b32_e32 v5, 1, v5
	v_sub_u32_e32 v4, v6, v5
	v_mov_b32_e32 v6, 0x300
	v_lshl_or_b32 v7, v3, 2, v6
	v_mov_b32_e32 v6, 0
	s_mov_b64 s[10:11], 0
	v_mov_b32_e32 v9, v4
	v_mov_b32_e32 v8, 0

.LBB3_25:
	s_waitcnt vmcnt(3)
	s_add_i32 s67, s67, 1
	v_and_or_b32 v74, v58, v105, s19
	v_and_or_b32 v75, v59, v105, s19
	v_and_or_b32 v76, v60, v105, s19
	v_and_or_b32 v77, v61, v105, s19
	s_lshl_b64 s[24:25], s[8:9], 4
	ds_read_b128 v[240:243], v74
	ds_read_b128 v[98:101], v75
	ds_read_b128 v[94:97], v76
	ds_read_b128 v[74:77], v77
	s_waitcnt vmcnt(2)
	s_add_u32 s26, s45, s24
	v_and_or_b32 v78, v62, v105, s19
	v_and_or_b32 v79, v63, v105, s19
	v_and_or_b32 v80, v64, v105, s19
	v_and_or_b32 v81, v65, v105, s19
	s_addc_u32 s27, s46, s25
	ds_read_b128 v[90:93], v78
	ds_read_b128 v[86:89], v79
	ds_read_b128 v[82:85], v80
	ds_read_b128 v[78:81], v81
	s_waitcnt lgkmcnt(4)
	s_add_u32 s28, s47, s24
	v_fma_mix_f32 v182, v240, v58, v182 op_sel:[0,1,0] op_sel_hi:[1,1,0]
	v_fma_mix_f32 v183, v240, v58, v183 op_sel:[1,1,0] op_sel_hi:[1,1,0]
	v_fma_mix_f32 v184, v241, v58, v184 op_sel:[0,1,0] op_sel_hi:[1,1,0]
	v_fma_mix_f32 v185, v241, v58, v185 op_sel:[1,1,0] op_sel_hi:[1,1,0]
	v_fma_mix_f32 v186, v242, v58, v186 op_sel:[0,1,0] op_sel_hi:[1,1,0]
	v_fma_mix_f32 v187, v242, v58, v187 op_sel:[1,1,0] op_sel_hi:[1,1,0]
	v_fma_mix_f32 v188, v243, v58, v188 op_sel:[0,1,0] op_sel_hi:[1,1,0]
	v_fma_mix_f32 v189, v243, v58, v189 op_sel:[1,1,0] op_sel_hi:[1,1,0]
	v_fma_mix_f32 v182, v98, v59, v182 op_sel:[0,1,0] op_sel_hi:[1,1,0]
	v_fma_mix_f32 v183, v98, v59, v183 op_sel:[1,1,0] op_sel_hi:[1,1,0]
	v_fma_mix_f32 v184, v99, v59, v184 op_sel:[0,1,0] op_sel_hi:[1,1,0]
	v_fma_mix_f32 v185, v99, v59, v185 op_sel:[1,1,0] op_sel_hi:[1,1,0]
	v_fma_mix_f32 v186, v100, v59, v186 op_sel:[0,1,0] op_sel_hi:[1,1,0]
	v_fma_mix_f32 v187, v100, v59, v187 op_sel:[1,1,0] op_sel_hi:[1,1,0]
	v_fma_mix_f32 v188, v101, v59, v188 op_sel:[0,1,0] op_sel_hi:[1,1,0]
	v_fma_mix_f32 v189, v101, v59, v189 op_sel:[1,1,0] op_sel_hi:[1,1,0]
	v_fma_mix_f32 v182, v94, v60, v182 op_sel:[0,1,0] op_sel_hi:[1,1,0]
	v_fma_mix_f32 v183, v94, v60, v183 op_sel:[1,1,0] op_sel_hi:[1,1,0]
	v_fma_mix_f32 v184, v95, v60, v184 op_sel:[0,1,0] op_sel_hi:[1,1,0]
	v_fma_mix_f32 v185, v95, v60, v185 op_sel:[1,1,0] op_sel_hi:[1,1,0]
	v_fma_mix_f32 v186, v96, v60, v186 op_sel:[0,1,0] op_sel_hi:[1,1,0]
	v_fma_mix_f32 v187, v96, v60, v187 op_sel:[1,1,0] op_sel_hi:[1,1,0]
	v_fma_mix_f32 v188, v97, v60, v188 op_sel:[0,1,0] op_sel_hi:[1,1,0]
	v_fma_mix_f32 v189, v97, v60, v189 op_sel:[1,1,0] op_sel_hi:[1,1,0]
	v_fma_mix_f32 v182, v74, v61, v182 op_sel:[0,1,0] op_sel_hi:[1,1,0]
	v_fma_mix_f32 v183, v74, v61, v183 op_sel:[1,1,0] op_sel_hi:[1,1,0]
	v_fma_mix_f32 v184, v75, v61, v184 op_sel:[0,1,0] op_sel_hi:[1,1,0]
	v_fma_mix_f32 v185, v75, v61, v185 op_sel:[1,1,0] op_sel_hi:[1,1,0]
	v_fma_mix_f32 v186, v76, v61, v186 op_sel:[0,1,0] op_sel_hi:[1,1,0]
	v_fma_mix_f32 v187, v76, v61, v187 op_sel:[1,1,0] op_sel_hi:[1,1,0]
	v_fma_mix_f32 v188, v77, v61, v188 op_sel:[0,1,0] op_sel_hi:[1,1,0]
	v_fma_mix_f32 v189, v77, v61, v189 op_sel:[1,1,0] op_sel_hi:[1,1,0]
	global_load_dwordx4 v[58:61], v104, s[26:27]
	s_waitcnt vmcnt(2)
	s_addc_u32 s29, s48, s25
	v_and_or_b32 v74, v66, v105, s19
	v_and_or_b32 v94, v67, v105, s19
	v_and_or_b32 v98, v68, v105, s19
	v_and_or_b32 v240, v69, v105, s19
	s_add_u32 s30, s49, s24
	ds_read_b128 v[74:77], v74
	ds_read_b128 v[94:97], v94
	ds_read_b128 v[98:101], v98
	ds_read_b128 v[240:243], v240
	s_waitcnt lgkmcnt(4)
	s_addc_u32 s31, s50, s25
	v_fma_mix_f32 v198, v90, v62, v198 op_sel:[0,1,0] op_sel_hi:[1,1,0]
	v_fma_mix_f32 v199, v90, v62, v199 op_sel:[1,1,0] op_sel_hi:[1,1,0]
	v_fma_mix_f32 v200, v91, v62, v200 op_sel:[0,1,0] op_sel_hi:[1,1,0]
	v_fma_mix_f32 v201, v91, v62, v201 op_sel:[1,1,0] op_sel_hi:[1,1,0]
	v_fma_mix_f32 v202, v92, v62, v202 op_sel:[0,1,0] op_sel_hi:[1,1,0]
	v_fma_mix_f32 v203, v92, v62, v203 op_sel:[1,1,0] op_sel_hi:[1,1,0]
	v_fma_mix_f32 v204, v93, v62, v204 op_sel:[0,1,0] op_sel_hi:[1,1,0]
	v_fma_mix_f32 v205, v93, v62, v205 op_sel:[1,1,0] op_sel_hi:[1,1,0]
	v_fma_mix_f32 v198, v86, v63, v198 op_sel:[0,1,0] op_sel_hi:[1,1,0]
	v_fma_mix_f32 v199, v86, v63, v199 op_sel:[1,1,0] op_sel_hi:[1,1,0]
	v_fma_mix_f32 v200, v87, v63, v200 op_sel:[0,1,0] op_sel_hi:[1,1,0]
	v_fma_mix_f32 v201, v87, v63, v201 op_sel:[1,1,0] op_sel_hi:[1,1,0]
	v_fma_mix_f32 v202, v88, v63, v202 op_sel:[0,1,0] op_sel_hi:[1,1,0]
	v_fma_mix_f32 v203, v88, v63, v203 op_sel:[1,1,0] op_sel_hi:[1,1,0]
	v_fma_mix_f32 v204, v89, v63, v204 op_sel:[0,1,0] op_sel_hi:[1,1,0]
	v_fma_mix_f32 v205, v89, v63, v205 op_sel:[1,1,0] op_sel_hi:[1,1,0]
	v_fma_mix_f32 v198, v82, v64, v198 op_sel:[0,1,0] op_sel_hi:[1,1,0]
	v_fma_mix_f32 v199, v82, v64, v199 op_sel:[1,1,0] op_sel_hi:[1,1,0]
	v_fma_mix_f32 v200, v83, v64, v200 op_sel:[0,1,0] op_sel_hi:[1,1,0]
	v_fma_mix_f32 v201, v83, v64, v201 op_sel:[1,1,0] op_sel_hi:[1,1,0]
	v_fma_mix_f32 v202, v84, v64, v202 op_sel:[0,1,0] op_sel_hi:[1,1,0]
	v_fma_mix_f32 v203, v84, v64, v203 op_sel:[1,1,0] op_sel_hi:[1,1,0]
	v_fma_mix_f32 v204, v85, v64, v204 op_sel:[0,1,0] op_sel_hi:[1,1,0]
	v_fma_mix_f32 v205, v85, v64, v205 op_sel:[1,1,0] op_sel_hi:[1,1,0]
	v_fma_mix_f32 v198, v78, v65, v198 op_sel:[0,1,0] op_sel_hi:[1,1,0]
	v_fma_mix_f32 v199, v78, v65, v199 op_sel:[1,1,0] op_sel_hi:[1,1,0]
	v_fma_mix_f32 v200, v79, v65, v200 op_sel:[0,1,0] op_sel_hi:[1,1,0]
	v_fma_mix_f32 v201, v79, v65, v201 op_sel:[1,1,0] op_sel_hi:[1,1,0]
	v_fma_mix_f32 v202, v80, v65, v202 op_sel:[0,1,0] op_sel_hi:[1,1,0]
	v_fma_mix_f32 v203, v80, v65, v203 op_sel:[1,1,0] op_sel_hi:[1,1,0]
	v_fma_mix_f32 v204, v81, v65, v204 op_sel:[0,1,0] op_sel_hi:[1,1,0]
	v_fma_mix_f32 v205, v81, v65, v205 op_sel:[1,1,0] op_sel_hi:[1,1,0]
	global_load_dwordx4 v[62:65], v104, s[28:29]
	s_waitcnt vmcnt(2)
	s_add_u32 s24, s51, s24
	v_and_or_b32 v78, v70, v105, s19
	v_and_or_b32 v82, v71, v105, s19
	v_and_or_b32 v86, v72, v105, s19
	v_and_or_b32 v90, v73, v105, s19
	s_addc_u32 s25, s52, s25
	ds_read_b128 v[78:81], v78
	ds_read_b128 v[82:85], v82
	ds_read_b128 v[86:89], v86
	ds_read_b128 v[90:93], v90
	s_waitcnt lgkmcnt(4)
	s_add_i32 s8, s8, 64
	v_fma_mix_f32 v214, v74, v66, v214 op_sel:[0,1,0] op_sel_hi:[1,1,0]
	v_fma_mix_f32 v215, v74, v66, v215 op_sel:[1,1,0] op_sel_hi:[1,1,0]
	v_fma_mix_f32 v216, v75, v66, v216 op_sel:[0,1,0] op_sel_hi:[1,1,0]
	v_fma_mix_f32 v217, v75, v66, v217 op_sel:[1,1,0] op_sel_hi:[1,1,0]
	v_fma_mix_f32 v218, v76, v66, v218 op_sel:[0,1,0] op_sel_hi:[1,1,0]
	v_fma_mix_f32 v219, v76, v66, v219 op_sel:[1,1,0] op_sel_hi:[1,1,0]
	v_fma_mix_f32 v220, v77, v66, v220 op_sel:[0,1,0] op_sel_hi:[1,1,0]
	v_fma_mix_f32 v221, v77, v66, v221 op_sel:[1,1,0] op_sel_hi:[1,1,0]
	v_fma_mix_f32 v214, v94, v67, v214 op_sel:[0,1,0] op_sel_hi:[1,1,0]
	v_fma_mix_f32 v215, v94, v67, v215 op_sel:[1,1,0] op_sel_hi:[1,1,0]
	v_fma_mix_f32 v216, v95, v67, v216 op_sel:[0,1,0] op_sel_hi:[1,1,0]
	v_fma_mix_f32 v217, v95, v67, v217 op_sel:[1,1,0] op_sel_hi:[1,1,0]
	v_fma_mix_f32 v218, v96, v67, v218 op_sel:[0,1,0] op_sel_hi:[1,1,0]
	v_fma_mix_f32 v219, v96, v67, v219 op_sel:[1,1,0] op_sel_hi:[1,1,0]
	v_fma_mix_f32 v220, v97, v67, v220 op_sel:[0,1,0] op_sel_hi:[1,1,0]
	v_fma_mix_f32 v221, v97, v67, v221 op_sel:[1,1,0] op_sel_hi:[1,1,0]
	v_fma_mix_f32 v214, v98, v68, v214 op_sel:[0,1,0] op_sel_hi:[1,1,0]
	v_fma_mix_f32 v215, v98, v68, v215 op_sel:[1,1,0] op_sel_hi:[1,1,0]
	v_fma_mix_f32 v216, v99, v68, v216 op_sel:[0,1,0] op_sel_hi:[1,1,0]
	v_fma_mix_f32 v217, v99, v68, v217 op_sel:[1,1,0] op_sel_hi:[1,1,0]
	v_fma_mix_f32 v218, v100, v68, v218 op_sel:[0,1,0] op_sel_hi:[1,1,0]
	v_fma_mix_f32 v219, v100, v68, v219 op_sel:[1,1,0] op_sel_hi:[1,1,0]
	v_fma_mix_f32 v220, v101, v68, v220 op_sel:[0,1,0] op_sel_hi:[1,1,0]
	v_fma_mix_f32 v221, v101, v68, v221 op_sel:[1,1,0] op_sel_hi:[1,1,0]
	v_fma_mix_f32 v214, v240, v69, v214 op_sel:[0,1,0] op_sel_hi:[1,1,0]
	v_fma_mix_f32 v215, v240, v69, v215 op_sel:[1,1,0] op_sel_hi:[1,1,0]
	v_fma_mix_f32 v216, v241, v69, v216 op_sel:[0,1,0] op_sel_hi:[1,1,0]
	v_fma_mix_f32 v217, v241, v69, v217 op_sel:[1,1,0] op_sel_hi:[1,1,0]
	v_fma_mix_f32 v218, v242, v69, v218 op_sel:[0,1,0] op_sel_hi:[1,1,0]
	v_fma_mix_f32 v219, v242, v69, v219 op_sel:[1,1,0] op_sel_hi:[1,1,0]
	v_fma_mix_f32 v220, v243, v69, v220 op_sel:[0,1,0] op_sel_hi:[1,1,0]
	v_fma_mix_f32 v221, v243, v69, v221 op_sel:[1,1,0] op_sel_hi:[1,1,0]
	global_load_dwordx4 v[66:69], v104, s[30:31]
	s_waitcnt lgkmcnt(0)
	s_cmp_ge_i32 s67, s36
	v_fma_mix_f32 v222, v78, v70, v222 op_sel:[0,1,0] op_sel_hi:[1,1,0]
	v_fma_mix_f32 v223, v78, v70, v223 op_sel:[1,1,0] op_sel_hi:[1,1,0]
	v_fma_mix_f32 v224, v79, v70, v224 op_sel:[0,1,0] op_sel_hi:[1,1,0]
	v_fma_mix_f32 v225, v79, v70, v225 op_sel:[1,1,0] op_sel_hi:[1,1,0]
	v_fma_mix_f32 v226, v80, v70, v226 op_sel:[0,1,0] op_sel_hi:[1,1,0]
	v_fma_mix_f32 v227, v80, v70, v227 op_sel:[1,1,0] op_sel_hi:[1,1,0]
	v_fma_mix_f32 v228, v81, v70, v228 op_sel:[0,1,0] op_sel_hi:[1,1,0]
	v_fma_mix_f32 v229, v81, v70, v229 op_sel:[1,1,0] op_sel_hi:[1,1,0]
	v_fma_mix_f32 v222, v82, v71, v222 op_sel:[0,1,0] op_sel_hi:[1,1,0]
	v_fma_mix_f32 v223, v82, v71, v223 op_sel:[1,1,0] op_sel_hi:[1,1,0]
	v_fma_mix_f32 v224, v83, v71, v224 op_sel:[0,1,0] op_sel_hi:[1,1,0]
	v_fma_mix_f32 v225, v83, v71, v225 op_sel:[1,1,0] op_sel_hi:[1,1,0]
	v_fma_mix_f32 v226, v84, v71, v226 op_sel:[0,1,0] op_sel_hi:[1,1,0]
	v_fma_mix_f32 v227, v84, v71, v227 op_sel:[1,1,0] op_sel_hi:[1,1,0]
	v_fma_mix_f32 v228, v85, v71, v228 op_sel:[0,1,0] op_sel_hi:[1,1,0]
	v_fma_mix_f32 v229, v85, v71, v229 op_sel:[1,1,0] op_sel_hi:[1,1,0]
	v_fma_mix_f32 v222, v86, v72, v222 op_sel:[0,1,0] op_sel_hi:[1,1,0]
	v_fma_mix_f32 v223, v86, v72, v223 op_sel:[1,1,0] op_sel_hi:[1,1,0]
	v_fma_mix_f32 v224, v87, v72, v224 op_sel:[0,1,0] op_sel_hi:[1,1,0]
	v_fma_mix_f32 v225, v87, v72, v225 op_sel:[1,1,0] op_sel_hi:[1,1,0]
	v_fma_mix_f32 v226, v88, v72, v226 op_sel:[0,1,0] op_sel_hi:[1,1,0]
	v_fma_mix_f32 v227, v88, v72, v227 op_sel:[1,1,0] op_sel_hi:[1,1,0]
	v_fma_mix_f32 v228, v89, v72, v228 op_sel:[0,1,0] op_sel_hi:[1,1,0]
	v_fma_mix_f32 v229, v89, v72, v229 op_sel:[1,1,0] op_sel_hi:[1,1,0]
	v_fma_mix_f32 v222, v90, v73, v222 op_sel:[0,1,0] op_sel_hi:[1,1,0]
	v_fma_mix_f32 v223, v90, v73, v223 op_sel:[1,1,0] op_sel_hi:[1,1,0]
	v_fma_mix_f32 v224, v91, v73, v224 op_sel:[0,1,0] op_sel_hi:[1,1,0]
	v_fma_mix_f32 v225, v91, v73, v225 op_sel:[1,1,0] op_sel_hi:[1,1,0]
	v_fma_mix_f32 v226, v92, v73, v226 op_sel:[0,1,0] op_sel_hi:[1,1,0]
	v_fma_mix_f32 v227, v92, v73, v227 op_sel:[1,1,0] op_sel_hi:[1,1,0]
	v_fma_mix_f32 v228, v93, v73, v228 op_sel:[0,1,0] op_sel_hi:[1,1,0]
	v_fma_mix_f32 v229, v93, v73, v229 op_sel:[1,1,0] op_sel_hi:[1,1,0]
	global_load_dwordx4 v[70:73], v104, s[24:25]
	s_cbranch_scc0 .LBB3_25

.LBB3_28:
	s_waitcnt vmcnt(2)
	s_ashr_i32 s25, s24, 31
	v_and_or_b32 v76, v62, v105, s19
	v_and_or_b32 v80, v63, v105, s19
	v_and_or_b32 v84, v64, v105, s19
	v_and_or_b32 v88, v65, v105, s19
	s_add_i32 s8, s8, 1
	ds_read_b128 v[76:79], v76
	ds_read_b128 v[80:83], v80
	ds_read_b128 v[84:87], v84
	ds_read_b128 v[88:91], v88
	s_lshl_b64 s[26:27], s[24:25], 4
	s_waitcnt lgkmcnt(0)
	s_add_u32 s28, s47, s26
	v_fma_mix_f32 v198, v76, v62, v198 op_sel:[0,1,0] op_sel_hi:[1,1,0]
	v_fma_mix_f32 v199, v76, v62, v199 op_sel:[1,1,0] op_sel_hi:[1,1,0]
	v_fma_mix_f32 v200, v77, v62, v200 op_sel:[0,1,0] op_sel_hi:[1,1,0]
	v_fma_mix_f32 v201, v77, v62, v201 op_sel:[1,1,0] op_sel_hi:[1,1,0]
	v_fma_mix_f32 v202, v78, v62, v202 op_sel:[0,1,0] op_sel_hi:[1,1,0]
	v_fma_mix_f32 v203, v78, v62, v203 op_sel:[1,1,0] op_sel_hi:[1,1,0]
	v_fma_mix_f32 v204, v79, v62, v204 op_sel:[0,1,0] op_sel_hi:[1,1,0]
	v_fma_mix_f32 v205, v79, v62, v205 op_sel:[1,1,0] op_sel_hi:[1,1,0]
	v_fma_mix_f32 v198, v80, v63, v198 op_sel:[0,1,0] op_sel_hi:[1,1,0]
	v_fma_mix_f32 v199, v80, v63, v199 op_sel:[1,1,0] op_sel_hi:[1,1,0]
	v_fma_mix_f32 v200, v81, v63, v200 op_sel:[0,1,0] op_sel_hi:[1,1,0]
	v_fma_mix_f32 v201, v81, v63, v201 op_sel:[1,1,0] op_sel_hi:[1,1,0]
	v_fma_mix_f32 v202, v82, v63, v202 op_sel:[0,1,0] op_sel_hi:[1,1,0]
	v_fma_mix_f32 v203, v82, v63, v203 op_sel:[1,1,0] op_sel_hi:[1,1,0]
	v_fma_mix_f32 v204, v83, v63, v204 op_sel:[0,1,0] op_sel_hi:[1,1,0]
	v_fma_mix_f32 v205, v83, v63, v205 op_sel:[1,1,0] op_sel_hi:[1,1,0]
	v_fma_mix_f32 v198, v84, v64, v198 op_sel:[0,1,0] op_sel_hi:[1,1,0]
	v_fma_mix_f32 v199, v84, v64, v199 op_sel:[1,1,0] op_sel_hi:[1,1,0]
	v_fma_mix_f32 v200, v85, v64, v200 op_sel:[0,1,0] op_sel_hi:[1,1,0]
	v_fma_mix_f32 v201, v85, v64, v201 op_sel:[1,1,0] op_sel_hi:[1,1,0]
	v_fma_mix_f32 v202, v86, v64, v202 op_sel:[0,1,0] op_sel_hi:[1,1,0]
	v_fma_mix_f32 v203, v86, v64, v203 op_sel:[1,1,0] op_sel_hi:[1,1,0]
	v_fma_mix_f32 v204, v87, v64, v204 op_sel:[0,1,0] op_sel_hi:[1,1,0]
	v_fma_mix_f32 v205, v87, v64, v205 op_sel:[1,1,0] op_sel_hi:[1,1,0]
	v_fma_mix_f32 v198, v88, v65, v198 op_sel:[0,1,0] op_sel_hi:[1,1,0]
	v_fma_mix_f32 v199, v88, v65, v199 op_sel:[1,1,0] op_sel_hi:[1,1,0]
	v_fma_mix_f32 v200, v89, v65, v200 op_sel:[0,1,0] op_sel_hi:[1,1,0]
	v_fma_mix_f32 v201, v89, v65, v201 op_sel:[1,1,0] op_sel_hi:[1,1,0]
	v_fma_mix_f32 v202, v90, v65, v202 op_sel:[0,1,0] op_sel_hi:[1,1,0]
	v_fma_mix_f32 v203, v90, v65, v203 op_sel:[1,1,0] op_sel_hi:[1,1,0]
	v_fma_mix_f32 v204, v91, v65, v204 op_sel:[0,1,0] op_sel_hi:[1,1,0]
	v_fma_mix_f32 v205, v91, v65, v205 op_sel:[1,1,0] op_sel_hi:[1,1,0]
	s_addc_u32 s29, s48, s27
	global_load_dwordx4 v[62:65], v104, s[28:29]
	s_waitcnt vmcnt(2)
	s_add_u32 s28, s49, s26
	v_and_or_b32 v76, v66, v105, s19
	v_and_or_b32 v80, v67, v105, s19
	v_and_or_b32 v84, v68, v105, s19
	v_and_or_b32 v88, v69, v105, s19
	s_addc_u32 s29, s50, s27
	ds_read_b128 v[76:79], v76
	ds_read_b128 v[80:83], v80
	ds_read_b128 v[84:87], v84
	ds_read_b128 v[88:91], v88
	s_add_u32 s26, s51, s26
	s_waitcnt lgkmcnt(0)
	s_addc_u32 s27, s52, s27
	v_fma_mix_f32 v214, v76, v66, v214 op_sel:[0,1,0] op_sel_hi:[1,1,0]
	v_fma_mix_f32 v215, v76, v66, v215 op_sel:[1,1,0] op_sel_hi:[1,1,0]
	v_fma_mix_f32 v216, v77, v66, v216 op_sel:[0,1,0] op_sel_hi:[1,1,0]
	v_fma_mix_f32 v217, v77, v66, v217 op_sel:[1,1,0] op_sel_hi:[1,1,0]
	v_fma_mix_f32 v218, v78, v66, v218 op_sel:[0,1,0] op_sel_hi:[1,1,0]
	v_fma_mix_f32 v219, v78, v66, v219 op_sel:[1,1,0] op_sel_hi:[1,1,0]
	v_fma_mix_f32 v220, v79, v66, v220 op_sel:[0,1,0] op_sel_hi:[1,1,0]
	v_fma_mix_f32 v221, v79, v66, v221 op_sel:[1,1,0] op_sel_hi:[1,1,0]
	v_fma_mix_f32 v214, v80, v67, v214 op_sel:[0,1,0] op_sel_hi:[1,1,0]
	v_fma_mix_f32 v215, v80, v67, v215 op_sel:[1,1,0] op_sel_hi:[1,1,0]
	v_fma_mix_f32 v216, v81, v67, v216 op_sel:[0,1,0] op_sel_hi:[1,1,0]
	v_fma_mix_f32 v217, v81, v67, v217 op_sel:[1,1,0] op_sel_hi:[1,1,0]
	v_fma_mix_f32 v218, v82, v67, v218 op_sel:[0,1,0] op_sel_hi:[1,1,0]
	v_fma_mix_f32 v219, v82, v67, v219 op_sel:[1,1,0] op_sel_hi:[1,1,0]
	v_fma_mix_f32 v220, v83, v67, v220 op_sel:[0,1,0] op_sel_hi:[1,1,0]
	v_fma_mix_f32 v221, v83, v67, v221 op_sel:[1,1,0] op_sel_hi:[1,1,0]
	v_fma_mix_f32 v214, v84, v68, v214 op_sel:[0,1,0] op_sel_hi:[1,1,0]
	v_fma_mix_f32 v215, v84, v68, v215 op_sel:[1,1,0] op_sel_hi:[1,1,0]
	v_fma_mix_f32 v216, v85, v68, v216 op_sel:[0,1,0] op_sel_hi:[1,1,0]
	v_fma_mix_f32 v217, v85, v68, v217 op_sel:[1,1,0] op_sel_hi:[1,1,0]
	v_fma_mix_f32 v218, v86, v68, v218 op_sel:[0,1,0] op_sel_hi:[1,1,0]
	v_fma_mix_f32 v219, v86, v68, v219 op_sel:[1,1,0] op_sel_hi:[1,1,0]
	v_fma_mix_f32 v220, v87, v68, v220 op_sel:[0,1,0] op_sel_hi:[1,1,0]
	v_fma_mix_f32 v221, v87, v68, v221 op_sel:[1,1,0] op_sel_hi:[1,1,0]
	v_fma_mix_f32 v214, v88, v69, v214 op_sel:[0,1,0] op_sel_hi:[1,1,0]
	v_fma_mix_f32 v215, v88, v69, v215 op_sel:[1,1,0] op_sel_hi:[1,1,0]
	v_fma_mix_f32 v216, v89, v69, v216 op_sel:[0,1,0] op_sel_hi:[1,1,0]
	v_fma_mix_f32 v217, v89, v69, v217 op_sel:[1,1,0] op_sel_hi:[1,1,0]
	v_fma_mix_f32 v218, v90, v69, v218 op_sel:[0,1,0] op_sel_hi:[1,1,0]
	v_fma_mix_f32 v219, v90, v69, v219 op_sel:[1,1,0] op_sel_hi:[1,1,0]
	v_fma_mix_f32 v220, v91, v69, v220 op_sel:[0,1,0] op_sel_hi:[1,1,0]
	v_fma_mix_f32 v221, v91, v69, v221 op_sel:[1,1,0] op_sel_hi:[1,1,0]
	global_load_dwordx4 v[66:69], v104, s[28:29]
	s_waitcnt vmcnt(2)
	s_add_i32 s24, s24, 64
	v_and_or_b32 v76, v70, v105, s19
	v_and_or_b32 v80, v71, v105, s19
	v_and_or_b32 v84, v72, v105, s19
	v_and_or_b32 v88, v73, v105, s19
	s_cmp_ge_i32 s8, s35
	ds_read_b128 v[76:79], v76
	ds_read_b128 v[80:83], v80
	ds_read_b128 v[84:87], v84
	ds_read_b128 v[88:91], v88
	s_nop 0
	s_waitcnt lgkmcnt(0)
	s_nop 0
	v_fma_mix_f32 v222, v76, v70, v222 op_sel:[0,1,0] op_sel_hi:[1,1,0]
	v_fma_mix_f32 v223, v76, v70, v223 op_sel:[1,1,0] op_sel_hi:[1,1,0]
	v_fma_mix_f32 v224, v77, v70, v224 op_sel:[0,1,0] op_sel_hi:[1,1,0]
	v_fma_mix_f32 v225, v77, v70, v225 op_sel:[1,1,0] op_sel_hi:[1,1,0]
	v_fma_mix_f32 v226, v78, v70, v226 op_sel:[0,1,0] op_sel_hi:[1,1,0]
	v_fma_mix_f32 v227, v78, v70, v227 op_sel:[1,1,0] op_sel_hi:[1,1,0]
	v_fma_mix_f32 v228, v79, v70, v228 op_sel:[0,1,0] op_sel_hi:[1,1,0]
	v_fma_mix_f32 v229, v79, v70, v229 op_sel:[1,1,0] op_sel_hi:[1,1,0]
	v_fma_mix_f32 v222, v80, v71, v222 op_sel:[0,1,0] op_sel_hi:[1,1,0]
	v_fma_mix_f32 v223, v80, v71, v223 op_sel:[1,1,0] op_sel_hi:[1,1,0]
	v_fma_mix_f32 v224, v81, v71, v224 op_sel:[0,1,0] op_sel_hi:[1,1,0]
	v_fma_mix_f32 v225, v81, v71, v225 op_sel:[1,1,0] op_sel_hi:[1,1,0]
	v_fma_mix_f32 v226, v82, v71, v226 op_sel:[0,1,0] op_sel_hi:[1,1,0]
	v_fma_mix_f32 v227, v82, v71, v227 op_sel:[1,1,0] op_sel_hi:[1,1,0]
	v_fma_mix_f32 v228, v83, v71, v228 op_sel:[0,1,0] op_sel_hi:[1,1,0]
	v_fma_mix_f32 v229, v83, v71, v229 op_sel:[1,1,0] op_sel_hi:[1,1,0]
	v_fma_mix_f32 v222, v84, v72, v222 op_sel:[0,1,0] op_sel_hi:[1,1,0]
	v_fma_mix_f32 v223, v84, v72, v223 op_sel:[1,1,0] op_sel_hi:[1,1,0]
	v_fma_mix_f32 v224, v85, v72, v224 op_sel:[0,1,0] op_sel_hi:[1,1,0]
	v_fma_mix_f32 v225, v85, v72, v225 op_sel:[1,1,0] op_sel_hi:[1,1,0]
	v_fma_mix_f32 v226, v86, v72, v226 op_sel:[0,1,0] op_sel_hi:[1,1,0]
	v_fma_mix_f32 v227, v86, v72, v227 op_sel:[1,1,0] op_sel_hi:[1,1,0]
	v_fma_mix_f32 v228, v87, v72, v228 op_sel:[0,1,0] op_sel_hi:[1,1,0]
	v_fma_mix_f32 v229, v87, v72, v229 op_sel:[1,1,0] op_sel_hi:[1,1,0]
	v_fma_mix_f32 v222, v88, v73, v222 op_sel:[0,1,0] op_sel_hi:[1,1,0]
	v_fma_mix_f32 v223, v88, v73, v223 op_sel:[1,1,0] op_sel_hi:[1,1,0]
	v_fma_mix_f32 v224, v89, v73, v224 op_sel:[0,1,0] op_sel_hi:[1,1,0]
	v_fma_mix_f32 v225, v89, v73, v225 op_sel:[1,1,0] op_sel_hi:[1,1,0]
	v_fma_mix_f32 v226, v90, v73, v226 op_sel:[0,1,0] op_sel_hi:[1,1,0]
	v_fma_mix_f32 v227, v90, v73, v227 op_sel:[1,1,0] op_sel_hi:[1,1,0]
	v_fma_mix_f32 v228, v91, v73, v228 op_sel:[0,1,0] op_sel_hi:[1,1,0]
	v_fma_mix_f32 v229, v91, v73, v229 op_sel:[1,1,0] op_sel_hi:[1,1,0]
	global_load_dwordx4 v[70:73], v104, s[26:27]
	s_cbranch_scc0 .LBB3_28
	s_cmp_ge_i32 s8, s37
	s_cbranch_scc0 .LBB3_31
	s_branch .LBB3_33

.LBB3_32:
	s_waitcnt vmcnt(1)
	s_ashr_i32 s25, s24, 31
	v_and_or_b32 v76, v66, v105, s19
	v_and_or_b32 v80, v67, v105, s19
	v_and_or_b32 v84, v68, v105, s19
	v_and_or_b32 v88, v69, v105, s19
	s_add_i32 s8, s8, 1
	ds_read_b128 v[76:79], v76
	ds_read_b128 v[80:83], v80
	ds_read_b128 v[84:87], v84
	ds_read_b128 v[88:91], v88
	s_lshl_b64 s[26:27], s[24:25], 4
	s_waitcnt lgkmcnt(0)
	s_add_u32 s28, s49, s26
	v_fma_mix_f32 v214, v76, v66, v214 op_sel:[0,1,0] op_sel_hi:[1,1,0]
	v_fma_mix_f32 v215, v76, v66, v215 op_sel:[1,1,0] op_sel_hi:[1,1,0]
	v_fma_mix_f32 v216, v77, v66, v216 op_sel:[0,1,0] op_sel_hi:[1,1,0]
	v_fma_mix_f32 v217, v77, v66, v217 op_sel:[1,1,0] op_sel_hi:[1,1,0]
	v_fma_mix_f32 v218, v78, v66, v218 op_sel:[0,1,0] op_sel_hi:[1,1,0]
	v_fma_mix_f32 v219, v78, v66, v219 op_sel:[1,1,0] op_sel_hi:[1,1,0]
	v_fma_mix_f32 v220, v79, v66, v220 op_sel:[0,1,0] op_sel_hi:[1,1,0]
	v_fma_mix_f32 v221, v79, v66, v221 op_sel:[1,1,0] op_sel_hi:[1,1,0]
	v_fma_mix_f32 v214, v80, v67, v214 op_sel:[0,1,0] op_sel_hi:[1,1,0]
	v_fma_mix_f32 v215, v80, v67, v215 op_sel:[1,1,0] op_sel_hi:[1,1,0]
	v_fma_mix_f32 v216, v81, v67, v216 op_sel:[0,1,0] op_sel_hi:[1,1,0]
	v_fma_mix_f32 v217, v81, v67, v217 op_sel:[1,1,0] op_sel_hi:[1,1,0]
	v_fma_mix_f32 v218, v82, v67, v218 op_sel:[0,1,0] op_sel_hi:[1,1,0]
	v_fma_mix_f32 v219, v82, v67, v219 op_sel:[1,1,0] op_sel_hi:[1,1,0]
	v_fma_mix_f32 v220, v83, v67, v220 op_sel:[0,1,0] op_sel_hi:[1,1,0]
	v_fma_mix_f32 v221, v83, v67, v221 op_sel:[1,1,0] op_sel_hi:[1,1,0]
	v_fma_mix_f32 v214, v84, v68, v214 op_sel:[0,1,0] op_sel_hi:[1,1,0]
	v_fma_mix_f32 v215, v84, v68, v215 op_sel:[1,1,0] op_sel_hi:[1,1,0]
	v_fma_mix_f32 v216, v85, v68, v216 op_sel:[0,1,0] op_sel_hi:[1,1,0]
	v_fma_mix_f32 v217, v85, v68, v217 op_sel:[1,1,0] op_sel_hi:[1,1,0]
	v_fma_mix_f32 v218, v86, v68, v218 op_sel:[0,1,0] op_sel_hi:[1,1,0]
	v_fma_mix_f32 v219, v86, v68, v219 op_sel:[1,1,0] op_sel_hi:[1,1,0]
	v_fma_mix_f32 v220, v87, v68, v220 op_sel:[0,1,0] op_sel_hi:[1,1,0]
	v_fma_mix_f32 v221, v87, v68, v221 op_sel:[1,1,0] op_sel_hi:[1,1,0]
	v_fma_mix_f32 v214, v88, v69, v214 op_sel:[0,1,0] op_sel_hi:[1,1,0]
	v_fma_mix_f32 v215, v88, v69, v215 op_sel:[1,1,0] op_sel_hi:[1,1,0]
	v_fma_mix_f32 v216, v89, v69, v216 op_sel:[0,1,0] op_sel_hi:[1,1,0]
	v_fma_mix_f32 v217, v89, v69, v217 op_sel:[1,1,0] op_sel_hi:[1,1,0]
	v_fma_mix_f32 v218, v90, v69, v218 op_sel:[0,1,0] op_sel_hi:[1,1,0]
	v_fma_mix_f32 v219, v90, v69, v219 op_sel:[1,1,0] op_sel_hi:[1,1,0]
	v_fma_mix_f32 v220, v91, v69, v220 op_sel:[0,1,0] op_sel_hi:[1,1,0]
	v_fma_mix_f32 v221, v91, v69, v221 op_sel:[1,1,0] op_sel_hi:[1,1,0]
	s_addc_u32 s29, s50, s27
	global_load_dwordx4 v[66:69], v104, s[28:29]
	s_waitcnt vmcnt(1)
	s_add_u32 s26, s51, s26
	v_and_or_b32 v76, v70, v105, s19
	v_and_or_b32 v80, v71, v105, s19
	v_and_or_b32 v84, v72, v105, s19
	v_and_or_b32 v88, v73, v105, s19
	s_addc_u32 s27, s52, s27
	ds_read_b128 v[76:79], v76
	ds_read_b128 v[80:83], v80
	ds_read_b128 v[84:87], v84
	ds_read_b128 v[88:91], v88
	s_add_i32 s24, s24, 64
	s_waitcnt lgkmcnt(0)
	s_cmp_ge_i32 s8, s37
	v_fma_mix_f32 v222, v76, v70, v222 op_sel:[0,1,0] op_sel_hi:[1,1,0]
	v_fma_mix_f32 v223, v76, v70, v223 op_sel:[1,1,0] op_sel_hi:[1,1,0]
	v_fma_mix_f32 v224, v77, v70, v224 op_sel:[0,1,0] op_sel_hi:[1,1,0]
	v_fma_mix_f32 v225, v77, v70, v225 op_sel:[1,1,0] op_sel_hi:[1,1,0]
	v_fma_mix_f32 v226, v78, v70, v226 op_sel:[0,1,0] op_sel_hi:[1,1,0]
	v_fma_mix_f32 v227, v78, v70, v227 op_sel:[1,1,0] op_sel_hi:[1,1,0]
	v_fma_mix_f32 v228, v79, v70, v228 op_sel:[0,1,0] op_sel_hi:[1,1,0]
	v_fma_mix_f32 v229, v79, v70, v229 op_sel:[1,1,0] op_sel_hi:[1,1,0]
	v_fma_mix_f32 v222, v80, v71, v222 op_sel:[0,1,0] op_sel_hi:[1,1,0]
	v_fma_mix_f32 v223, v80, v71, v223 op_sel:[1,1,0] op_sel_hi:[1,1,0]
	v_fma_mix_f32 v224, v81, v71, v224 op_sel:[0,1,0] op_sel_hi:[1,1,0]
	v_fma_mix_f32 v225, v81, v71, v225 op_sel:[1,1,0] op_sel_hi:[1,1,0]
	v_fma_mix_f32 v226, v82, v71, v226 op_sel:[0,1,0] op_sel_hi:[1,1,0]
	v_fma_mix_f32 v227, v82, v71, v227 op_sel:[1,1,0] op_sel_hi:[1,1,0]
	v_fma_mix_f32 v228, v83, v71, v228 op_sel:[0,1,0] op_sel_hi:[1,1,0]
	v_fma_mix_f32 v229, v83, v71, v229 op_sel:[1,1,0] op_sel_hi:[1,1,0]
	v_fma_mix_f32 v222, v84, v72, v222 op_sel:[0,1,0] op_sel_hi:[1,1,0]
	v_fma_mix_f32 v223, v84, v72, v223 op_sel:[1,1,0] op_sel_hi:[1,1,0]
	v_fma_mix_f32 v224, v85, v72, v224 op_sel:[0,1,0] op_sel_hi:[1,1,0]
	v_fma_mix_f32 v225, v85, v72, v225 op_sel:[1,1,0] op_sel_hi:[1,1,0]
	v_fma_mix_f32 v226, v86, v72, v226 op_sel:[0,1,0] op_sel_hi:[1,1,0]
	v_fma_mix_f32 v227, v86, v72, v227 op_sel:[1,1,0] op_sel_hi:[1,1,0]
	v_fma_mix_f32 v228, v87, v72, v228 op_sel:[0,1,0] op_sel_hi:[1,1,0]
	v_fma_mix_f32 v229, v87, v72, v229 op_sel:[1,1,0] op_sel_hi:[1,1,0]
	v_fma_mix_f32 v222, v88, v73, v222 op_sel:[0,1,0] op_sel_hi:[1,1,0]
	v_fma_mix_f32 v223, v88, v73, v223 op_sel:[1,1,0] op_sel_hi:[1,1,0]
	v_fma_mix_f32 v224, v89, v73, v224 op_sel:[0,1,0] op_sel_hi:[1,1,0]
	v_fma_mix_f32 v225, v89, v73, v225 op_sel:[1,1,0] op_sel_hi:[1,1,0]
	v_fma_mix_f32 v226, v90, v73, v226 op_sel:[0,1,0] op_sel_hi:[1,1,0]
	v_fma_mix_f32 v227, v90, v73, v227 op_sel:[1,1,0] op_sel_hi:[1,1,0]
	v_fma_mix_f32 v228, v91, v73, v228 op_sel:[0,1,0] op_sel_hi:[1,1,0]
	v_fma_mix_f32 v229, v91, v73, v229 op_sel:[1,1,0] op_sel_hi:[1,1,0]
	global_load_dwordx4 v[70:73], v104, s[26:27]
	s_cbranch_scc0 .LBB3_32

.LBB3_35:
	s_waitcnt vmcnt(0)
	s_ashr_i32 s25, s24, 31
	v_and_or_b32 v76, v70, v105, s19
	v_and_or_b32 v80, v71, v105, s19
	v_and_or_b32 v84, v72, v105, s19
	v_and_or_b32 v88, v73, v105, s19
	s_add_i32 s8, s8, 1
	ds_read_b128 v[76:79], v76
	ds_read_b128 v[80:83], v80
	ds_read_b128 v[84:87], v84
	ds_read_b128 v[88:91], v88
	s_lshl_b64 s[26:27], s[24:25], 4
	s_waitcnt lgkmcnt(0)
	s_add_u32 s26, s51, s26
	v_fma_mix_f32 v222, v76, v70, v222 op_sel:[0,1,0] op_sel_hi:[1,1,0]
	v_fma_mix_f32 v223, v76, v70, v223 op_sel:[1,1,0] op_sel_hi:[1,1,0]
	v_fma_mix_f32 v224, v77, v70, v224 op_sel:[0,1,0] op_sel_hi:[1,1,0]
	v_fma_mix_f32 v225, v77, v70, v225 op_sel:[1,1,0] op_sel_hi:[1,1,0]
	v_fma_mix_f32 v226, v78, v70, v226 op_sel:[0,1,0] op_sel_hi:[1,1,0]
	v_fma_mix_f32 v227, v78, v70, v227 op_sel:[1,1,0] op_sel_hi:[1,1,0]
	v_fma_mix_f32 v228, v79, v70, v228 op_sel:[0,1,0] op_sel_hi:[1,1,0]
	v_fma_mix_f32 v229, v79, v70, v229 op_sel:[1,1,0] op_sel_hi:[1,1,0]
	v_fma_mix_f32 v222, v80, v71, v222 op_sel:[0,1,0] op_sel_hi:[1,1,0]
	v_fma_mix_f32 v223, v80, v71, v223 op_sel:[1,1,0] op_sel_hi:[1,1,0]
	v_fma_mix_f32 v224, v81, v71, v224 op_sel:[0,1,0] op_sel_hi:[1,1,0]
	v_fma_mix_f32 v225, v81, v71, v225 op_sel:[1,1,0] op_sel_hi:[1,1,0]
	v_fma_mix_f32 v226, v82, v71, v226 op_sel:[0,1,0] op_sel_hi:[1,1,0]
	v_fma_mix_f32 v227, v82, v71, v227 op_sel:[1,1,0] op_sel_hi:[1,1,0]
	v_fma_mix_f32 v228, v83, v71, v228 op_sel:[0,1,0] op_sel_hi:[1,1,0]
	v_fma_mix_f32 v229, v83, v71, v229 op_sel:[1,1,0] op_sel_hi:[1,1,0]
	s_addc_u32 s27, s52, s27
	s_add_i32 s24, s24, 64
	v_fma_mix_f32 v222, v84, v72, v222 op_sel:[0,1,0] op_sel_hi:[1,1,0]
	v_fma_mix_f32 v223, v84, v72, v223 op_sel:[1,1,0] op_sel_hi:[1,1,0]
	v_fma_mix_f32 v224, v85, v72, v224 op_sel:[0,1,0] op_sel_hi:[1,1,0]
	v_fma_mix_f32 v225, v85, v72, v225 op_sel:[1,1,0] op_sel_hi:[1,1,0]
	v_fma_mix_f32 v226, v86, v72, v226 op_sel:[0,1,0] op_sel_hi:[1,1,0]
	v_fma_mix_f32 v227, v86, v72, v227 op_sel:[1,1,0] op_sel_hi:[1,1,0]
	v_fma_mix_f32 v228, v87, v72, v228 op_sel:[0,1,0] op_sel_hi:[1,1,0]
	v_fma_mix_f32 v229, v87, v72, v229 op_sel:[1,1,0] op_sel_hi:[1,1,0]
	s_cmp_lt_i32 s8, s38
	v_fma_mix_f32 v222, v88, v73, v222 op_sel:[0,1,0] op_sel_hi:[1,1,0]
	v_fma_mix_f32 v223, v88, v73, v223 op_sel:[1,1,0] op_sel_hi:[1,1,0]
	v_fma_mix_f32 v224, v89, v73, v224 op_sel:[0,1,0] op_sel_hi:[1,1,0]
	v_fma_mix_f32 v225, v89, v73, v225 op_sel:[1,1,0] op_sel_hi:[1,1,0]
	v_fma_mix_f32 v226, v90, v73, v226 op_sel:[0,1,0] op_sel_hi:[1,1,0]
	v_fma_mix_f32 v227, v90, v73, v227 op_sel:[1,1,0] op_sel_hi:[1,1,0]
	v_fma_mix_f32 v228, v91, v73, v228 op_sel:[0,1,0] op_sel_hi:[1,1,0]
	v_fma_mix_f32 v229, v91, v73, v229 op_sel:[1,1,0] op_sel_hi:[1,1,0]
	global_load_dwordx4 v[70:73], v104, s[26:27]
	s_cbranch_scc1 .LBB3_35

.LBB3_40:
	s_waitcnt vmcnt(3)
	s_add_i32 s68, s68, 1
	v_and_or_b32 v74, v58, v105, s19
	v_and_or_b32 v75, v59, v105, s19
	v_and_or_b32 v76, v60, v105, s19
	v_and_or_b32 v77, v61, v105, s19
	s_lshl_b64 s[24:25], s[8:9], 4
	ds_read_b128 v[242:245], v74
	ds_read_b128 v[98:101], v75
	ds_read_b128 v[94:97], v76
	ds_read_b128 v[74:77], v77
	s_waitcnt vmcnt(2)
	s_add_u32 s26, s53, s24
	v_and_or_b32 v78, v62, v105, s19
	v_and_or_b32 v79, v63, v105, s19
	v_and_or_b32 v80, v64, v105, s19
	v_and_or_b32 v81, v65, v105, s19
	s_addc_u32 s27, s54, s25
	ds_read_b128 v[90:93], v78
	ds_read_b128 v[86:89], v79
	ds_read_b128 v[82:85], v80
	ds_read_b128 v[78:81], v81
	s_waitcnt lgkmcnt(4)
	s_add_u32 s28, s55, s24
	v_fma_mix_f32 v206, v242, v58, v206 op_sel:[0,1,0] op_sel_hi:[1,1,0]
	v_fma_mix_f32 v207, v242, v58, v207 op_sel:[1,1,0] op_sel_hi:[1,1,0]
	v_fma_mix_f32 v208, v243, v58, v208 op_sel:[0,1,0] op_sel_hi:[1,1,0]
	v_fma_mix_f32 v209, v243, v58, v209 op_sel:[1,1,0] op_sel_hi:[1,1,0]
	v_fma_mix_f32 v210, v244, v58, v210 op_sel:[0,1,0] op_sel_hi:[1,1,0]
	v_fma_mix_f32 v211, v244, v58, v211 op_sel:[1,1,0] op_sel_hi:[1,1,0]
	v_fma_mix_f32 v212, v245, v58, v212 op_sel:[0,1,0] op_sel_hi:[1,1,0]
	v_fma_mix_f32 v213, v245, v58, v213 op_sel:[1,1,0] op_sel_hi:[1,1,0]
	v_fma_mix_f32 v206, v98, v59, v206 op_sel:[0,1,0] op_sel_hi:[1,1,0]
	v_fma_mix_f32 v207, v98, v59, v207 op_sel:[1,1,0] op_sel_hi:[1,1,0]
	v_fma_mix_f32 v208, v99, v59, v208 op_sel:[0,1,0] op_sel_hi:[1,1,0]
	v_fma_mix_f32 v209, v99, v59, v209 op_sel:[1,1,0] op_sel_hi:[1,1,0]
	v_fma_mix_f32 v210, v100, v59, v210 op_sel:[0,1,0] op_sel_hi:[1,1,0]
	v_fma_mix_f32 v211, v100, v59, v211 op_sel:[1,1,0] op_sel_hi:[1,1,0]
	v_fma_mix_f32 v212, v101, v59, v212 op_sel:[0,1,0] op_sel_hi:[1,1,0]
	v_fma_mix_f32 v213, v101, v59, v213 op_sel:[1,1,0] op_sel_hi:[1,1,0]
	v_fma_mix_f32 v206, v94, v60, v206 op_sel:[0,1,0] op_sel_hi:[1,1,0]
	v_fma_mix_f32 v207, v94, v60, v207 op_sel:[1,1,0] op_sel_hi:[1,1,0]
	v_fma_mix_f32 v208, v95, v60, v208 op_sel:[0,1,0] op_sel_hi:[1,1,0]
	v_fma_mix_f32 v209, v95, v60, v209 op_sel:[1,1,0] op_sel_hi:[1,1,0]
	v_fma_mix_f32 v210, v96, v60, v210 op_sel:[0,1,0] op_sel_hi:[1,1,0]
	v_fma_mix_f32 v211, v96, v60, v211 op_sel:[1,1,0] op_sel_hi:[1,1,0]
	v_fma_mix_f32 v212, v97, v60, v212 op_sel:[0,1,0] op_sel_hi:[1,1,0]
	v_fma_mix_f32 v213, v97, v60, v213 op_sel:[1,1,0] op_sel_hi:[1,1,0]
	v_fma_mix_f32 v206, v74, v61, v206 op_sel:[0,1,0] op_sel_hi:[1,1,0]
	v_fma_mix_f32 v207, v74, v61, v207 op_sel:[1,1,0] op_sel_hi:[1,1,0]
	v_fma_mix_f32 v208, v75, v61, v208 op_sel:[0,1,0] op_sel_hi:[1,1,0]
	v_fma_mix_f32 v209, v75, v61, v209 op_sel:[1,1,0] op_sel_hi:[1,1,0]
	v_fma_mix_f32 v210, v76, v61, v210 op_sel:[0,1,0] op_sel_hi:[1,1,0]
	v_fma_mix_f32 v211, v76, v61, v211 op_sel:[1,1,0] op_sel_hi:[1,1,0]
	v_fma_mix_f32 v212, v77, v61, v212 op_sel:[0,1,0] op_sel_hi:[1,1,0]
	v_fma_mix_f32 v213, v77, v61, v213 op_sel:[1,1,0] op_sel_hi:[1,1,0]
	global_load_dwordx4 v[58:61], v104, s[26:27]
	s_waitcnt vmcnt(2)
	s_addc_u32 s29, s56, s25
	v_and_or_b32 v74, v66, v105, s19
	v_and_or_b32 v94, v67, v105, s19
	v_and_or_b32 v98, v68, v105, s19
	v_and_or_b32 v231, v69, v105, s19
	s_add_u32 s30, s57, s24
	ds_read_b128 v[74:77], v74
	ds_read_b128 v[94:97], v94
	ds_read_b128 v[98:101], v98
	ds_read_b128 v[242:245], v231
	s_waitcnt lgkmcnt(4)
	s_addc_u32 s31, s58, s25
	v_fma_mix_f32 v190, v90, v62, v190 op_sel:[0,1,0] op_sel_hi:[1,1,0]
	v_fma_mix_f32 v191, v90, v62, v191 op_sel:[1,1,0] op_sel_hi:[1,1,0]
	v_fma_mix_f32 v192, v91, v62, v192 op_sel:[0,1,0] op_sel_hi:[1,1,0]
	v_fma_mix_f32 v193, v91, v62, v193 op_sel:[1,1,0] op_sel_hi:[1,1,0]
	v_fma_mix_f32 v194, v92, v62, v194 op_sel:[0,1,0] op_sel_hi:[1,1,0]
	v_fma_mix_f32 v195, v92, v62, v195 op_sel:[1,1,0] op_sel_hi:[1,1,0]
	v_fma_mix_f32 v196, v93, v62, v196 op_sel:[0,1,0] op_sel_hi:[1,1,0]
	v_fma_mix_f32 v197, v93, v62, v197 op_sel:[1,1,0] op_sel_hi:[1,1,0]
	v_fma_mix_f32 v190, v86, v63, v190 op_sel:[0,1,0] op_sel_hi:[1,1,0]
	v_fma_mix_f32 v191, v86, v63, v191 op_sel:[1,1,0] op_sel_hi:[1,1,0]
	v_fma_mix_f32 v192, v87, v63, v192 op_sel:[0,1,0] op_sel_hi:[1,1,0]
	v_fma_mix_f32 v193, v87, v63, v193 op_sel:[1,1,0] op_sel_hi:[1,1,0]
	v_fma_mix_f32 v194, v88, v63, v194 op_sel:[0,1,0] op_sel_hi:[1,1,0]
	v_fma_mix_f32 v195, v88, v63, v195 op_sel:[1,1,0] op_sel_hi:[1,1,0]
	v_fma_mix_f32 v196, v89, v63, v196 op_sel:[0,1,0] op_sel_hi:[1,1,0]
	v_fma_mix_f32 v197, v89, v63, v197 op_sel:[1,1,0] op_sel_hi:[1,1,0]
	v_fma_mix_f32 v190, v82, v64, v190 op_sel:[0,1,0] op_sel_hi:[1,1,0]
	v_fma_mix_f32 v191, v82, v64, v191 op_sel:[1,1,0] op_sel_hi:[1,1,0]
	v_fma_mix_f32 v192, v83, v64, v192 op_sel:[0,1,0] op_sel_hi:[1,1,0]
	v_fma_mix_f32 v193, v83, v64, v193 op_sel:[1,1,0] op_sel_hi:[1,1,0]
	v_fma_mix_f32 v194, v84, v64, v194 op_sel:[0,1,0] op_sel_hi:[1,1,0]
	v_fma_mix_f32 v195, v84, v64, v195 op_sel:[1,1,0] op_sel_hi:[1,1,0]
	v_fma_mix_f32 v196, v85, v64, v196 op_sel:[0,1,0] op_sel_hi:[1,1,0]
	v_fma_mix_f32 v197, v85, v64, v197 op_sel:[1,1,0] op_sel_hi:[1,1,0]
	v_fma_mix_f32 v190, v78, v65, v190 op_sel:[0,1,0] op_sel_hi:[1,1,0]
	v_fma_mix_f32 v191, v78, v65, v191 op_sel:[1,1,0] op_sel_hi:[1,1,0]
	v_fma_mix_f32 v192, v79, v65, v192 op_sel:[0,1,0] op_sel_hi:[1,1,0]
	v_fma_mix_f32 v193, v79, v65, v193 op_sel:[1,1,0] op_sel_hi:[1,1,0]
	v_fma_mix_f32 v194, v80, v65, v194 op_sel:[0,1,0] op_sel_hi:[1,1,0]
	v_fma_mix_f32 v195, v80, v65, v195 op_sel:[1,1,0] op_sel_hi:[1,1,0]
	v_fma_mix_f32 v196, v81, v65, v196 op_sel:[0,1,0] op_sel_hi:[1,1,0]
	v_fma_mix_f32 v197, v81, v65, v197 op_sel:[1,1,0] op_sel_hi:[1,1,0]
	global_load_dwordx4 v[62:65], v104, s[28:29]
	s_waitcnt vmcnt(2)
	s_add_u32 s24, s59, s24
	v_and_or_b32 v78, v70, v105, s19
	v_and_or_b32 v82, v71, v105, s19
	v_and_or_b32 v86, v72, v105, s19
	v_and_or_b32 v90, v73, v105, s19
	s_addc_u32 s25, s60, s25
	ds_read_b128 v[78:81], v78
	ds_read_b128 v[82:85], v82
	ds_read_b128 v[86:89], v86
	ds_read_b128 v[90:93], v90
	s_waitcnt lgkmcnt(4)
	s_add_i32 s8, s8, 64
	v_fma_mix_f32 v174, v74, v66, v174 op_sel:[0,1,0] op_sel_hi:[1,1,0]
	v_fma_mix_f32 v175, v74, v66, v175 op_sel:[1,1,0] op_sel_hi:[1,1,0]
	v_fma_mix_f32 v176, v75, v66, v176 op_sel:[0,1,0] op_sel_hi:[1,1,0]
	v_fma_mix_f32 v177, v75, v66, v177 op_sel:[1,1,0] op_sel_hi:[1,1,0]
	v_fma_mix_f32 v178, v76, v66, v178 op_sel:[0,1,0] op_sel_hi:[1,1,0]
	v_fma_mix_f32 v179, v76, v66, v179 op_sel:[1,1,0] op_sel_hi:[1,1,0]
	v_fma_mix_f32 v180, v77, v66, v180 op_sel:[0,1,0] op_sel_hi:[1,1,0]
	v_fma_mix_f32 v181, v77, v66, v181 op_sel:[1,1,0] op_sel_hi:[1,1,0]
	v_fma_mix_f32 v174, v94, v67, v174 op_sel:[0,1,0] op_sel_hi:[1,1,0]
	v_fma_mix_f32 v175, v94, v67, v175 op_sel:[1,1,0] op_sel_hi:[1,1,0]
	v_fma_mix_f32 v176, v95, v67, v176 op_sel:[0,1,0] op_sel_hi:[1,1,0]
	v_fma_mix_f32 v177, v95, v67, v177 op_sel:[1,1,0] op_sel_hi:[1,1,0]
	v_fma_mix_f32 v178, v96, v67, v178 op_sel:[0,1,0] op_sel_hi:[1,1,0]
	v_fma_mix_f32 v179, v96, v67, v179 op_sel:[1,1,0] op_sel_hi:[1,1,0]
	v_fma_mix_f32 v180, v97, v67, v180 op_sel:[0,1,0] op_sel_hi:[1,1,0]
	v_fma_mix_f32 v181, v97, v67, v181 op_sel:[1,1,0] op_sel_hi:[1,1,0]
	v_fma_mix_f32 v174, v98, v68, v174 op_sel:[0,1,0] op_sel_hi:[1,1,0]
	v_fma_mix_f32 v175, v98, v68, v175 op_sel:[1,1,0] op_sel_hi:[1,1,0]
	v_fma_mix_f32 v176, v99, v68, v176 op_sel:[0,1,0] op_sel_hi:[1,1,0]
	v_fma_mix_f32 v177, v99, v68, v177 op_sel:[1,1,0] op_sel_hi:[1,1,0]
	v_fma_mix_f32 v178, v100, v68, v178 op_sel:[0,1,0] op_sel_hi:[1,1,0]
	v_fma_mix_f32 v179, v100, v68, v179 op_sel:[1,1,0] op_sel_hi:[1,1,0]
	v_fma_mix_f32 v180, v101, v68, v180 op_sel:[0,1,0] op_sel_hi:[1,1,0]
	v_fma_mix_f32 v181, v101, v68, v181 op_sel:[1,1,0] op_sel_hi:[1,1,0]
	v_fma_mix_f32 v174, v242, v69, v174 op_sel:[0,1,0] op_sel_hi:[1,1,0]
	v_fma_mix_f32 v175, v242, v69, v175 op_sel:[1,1,0] op_sel_hi:[1,1,0]
	v_fma_mix_f32 v176, v243, v69, v176 op_sel:[0,1,0] op_sel_hi:[1,1,0]
	v_fma_mix_f32 v177, v243, v69, v177 op_sel:[1,1,0] op_sel_hi:[1,1,0]
	v_fma_mix_f32 v178, v244, v69, v178 op_sel:[0,1,0] op_sel_hi:[1,1,0]
	v_fma_mix_f32 v179, v244, v69, v179 op_sel:[1,1,0] op_sel_hi:[1,1,0]
	v_fma_mix_f32 v180, v245, v69, v180 op_sel:[0,1,0] op_sel_hi:[1,1,0]
	v_fma_mix_f32 v181, v245, v69, v181 op_sel:[1,1,0] op_sel_hi:[1,1,0]
	global_load_dwordx4 v[66:69], v104, s[30:31]
	s_waitcnt lgkmcnt(0)
	s_cmp_lt_i32 s68, s40
	v_fma_mix_f32 v166, v78, v70, v166 op_sel:[0,1,0] op_sel_hi:[1,1,0]
	v_fma_mix_f32 v167, v78, v70, v167 op_sel:[1,1,0] op_sel_hi:[1,1,0]
	v_fma_mix_f32 v168, v79, v70, v168 op_sel:[0,1,0] op_sel_hi:[1,1,0]
	v_fma_mix_f32 v169, v79, v70, v169 op_sel:[1,1,0] op_sel_hi:[1,1,0]
	v_fma_mix_f32 v170, v80, v70, v170 op_sel:[0,1,0] op_sel_hi:[1,1,0]
	v_fma_mix_f32 v171, v80, v70, v171 op_sel:[1,1,0] op_sel_hi:[1,1,0]
	v_fma_mix_f32 v172, v81, v70, v172 op_sel:[0,1,0] op_sel_hi:[1,1,0]
	v_fma_mix_f32 v173, v81, v70, v173 op_sel:[1,1,0] op_sel_hi:[1,1,0]
	v_fma_mix_f32 v166, v82, v71, v166 op_sel:[0,1,0] op_sel_hi:[1,1,0]
	v_fma_mix_f32 v167, v82, v71, v167 op_sel:[1,1,0] op_sel_hi:[1,1,0]
	v_fma_mix_f32 v168, v83, v71, v168 op_sel:[0,1,0] op_sel_hi:[1,1,0]
	v_fma_mix_f32 v169, v83, v71, v169 op_sel:[1,1,0] op_sel_hi:[1,1,0]
	v_fma_mix_f32 v170, v84, v71, v170 op_sel:[0,1,0] op_sel_hi:[1,1,0]
	v_fma_mix_f32 v171, v84, v71, v171 op_sel:[1,1,0] op_sel_hi:[1,1,0]
	v_fma_mix_f32 v172, v85, v71, v172 op_sel:[0,1,0] op_sel_hi:[1,1,0]
	v_fma_mix_f32 v173, v85, v71, v173 op_sel:[1,1,0] op_sel_hi:[1,1,0]
	v_fma_mix_f32 v166, v86, v72, v166 op_sel:[0,1,0] op_sel_hi:[1,1,0]
	v_fma_mix_f32 v167, v86, v72, v167 op_sel:[1,1,0] op_sel_hi:[1,1,0]
	v_fma_mix_f32 v168, v87, v72, v168 op_sel:[0,1,0] op_sel_hi:[1,1,0]
	v_fma_mix_f32 v169, v87, v72, v169 op_sel:[1,1,0] op_sel_hi:[1,1,0]
	v_fma_mix_f32 v170, v88, v72, v170 op_sel:[0,1,0] op_sel_hi:[1,1,0]
	v_fma_mix_f32 v171, v88, v72, v171 op_sel:[1,1,0] op_sel_hi:[1,1,0]
	v_fma_mix_f32 v172, v89, v72, v172 op_sel:[0,1,0] op_sel_hi:[1,1,0]
	v_fma_mix_f32 v173, v89, v72, v173 op_sel:[1,1,0] op_sel_hi:[1,1,0]
	v_fma_mix_f32 v166, v90, v73, v166 op_sel:[0,1,0] op_sel_hi:[1,1,0]
	v_fma_mix_f32 v167, v90, v73, v167 op_sel:[1,1,0] op_sel_hi:[1,1,0]
	v_fma_mix_f32 v168, v91, v73, v168 op_sel:[0,1,0] op_sel_hi:[1,1,0]
	v_fma_mix_f32 v169, v91, v73, v169 op_sel:[1,1,0] op_sel_hi:[1,1,0]
	v_fma_mix_f32 v170, v92, v73, v170 op_sel:[0,1,0] op_sel_hi:[1,1,0]
	v_fma_mix_f32 v171, v92, v73, v171 op_sel:[1,1,0] op_sel_hi:[1,1,0]
	v_fma_mix_f32 v172, v93, v73, v172 op_sel:[0,1,0] op_sel_hi:[1,1,0]
	v_fma_mix_f32 v173, v93, v73, v173 op_sel:[1,1,0] op_sel_hi:[1,1,0]
	global_load_dwordx4 v[70:73], v104, s[24:25]
	s_cbranch_scc1 .LBB3_40

.LBB3_43:
	s_waitcnt vmcnt(2)
	s_ashr_i32 s25, s24, 31
	v_and_or_b32 v74, v62, v105, s19
	v_and_or_b32 v78, v63, v105, s19
	v_and_or_b32 v82, v64, v105, s19
	v_and_or_b32 v86, v65, v105, s19
	s_add_i32 s8, s8, 1
	ds_read_b128 v[74:77], v74
	ds_read_b128 v[78:81], v78
	ds_read_b128 v[82:85], v82
	ds_read_b128 v[86:89], v86
	s_lshl_b64 s[26:27], s[24:25], 4
	s_waitcnt lgkmcnt(0)
	s_add_u32 s28, s55, s26
	v_fma_mix_f32 v190, v74, v62, v190 op_sel:[0,1,0] op_sel_hi:[1,1,0]
	v_fma_mix_f32 v191, v74, v62, v191 op_sel:[1,1,0] op_sel_hi:[1,1,0]
	v_fma_mix_f32 v192, v75, v62, v192 op_sel:[0,1,0] op_sel_hi:[1,1,0]
	v_fma_mix_f32 v193, v75, v62, v193 op_sel:[1,1,0] op_sel_hi:[1,1,0]
	v_fma_mix_f32 v194, v76, v62, v194 op_sel:[0,1,0] op_sel_hi:[1,1,0]
	v_fma_mix_f32 v195, v76, v62, v195 op_sel:[1,1,0] op_sel_hi:[1,1,0]
	v_fma_mix_f32 v196, v77, v62, v196 op_sel:[0,1,0] op_sel_hi:[1,1,0]
	v_fma_mix_f32 v197, v77, v62, v197 op_sel:[1,1,0] op_sel_hi:[1,1,0]
	v_fma_mix_f32 v190, v78, v63, v190 op_sel:[0,1,0] op_sel_hi:[1,1,0]
	v_fma_mix_f32 v191, v78, v63, v191 op_sel:[1,1,0] op_sel_hi:[1,1,0]
	v_fma_mix_f32 v192, v79, v63, v192 op_sel:[0,1,0] op_sel_hi:[1,1,0]
	v_fma_mix_f32 v193, v79, v63, v193 op_sel:[1,1,0] op_sel_hi:[1,1,0]
	v_fma_mix_f32 v194, v80, v63, v194 op_sel:[0,1,0] op_sel_hi:[1,1,0]
	v_fma_mix_f32 v195, v80, v63, v195 op_sel:[1,1,0] op_sel_hi:[1,1,0]
	v_fma_mix_f32 v196, v81, v63, v196 op_sel:[0,1,0] op_sel_hi:[1,1,0]
	v_fma_mix_f32 v197, v81, v63, v197 op_sel:[1,1,0] op_sel_hi:[1,1,0]
	v_fma_mix_f32 v190, v82, v64, v190 op_sel:[0,1,0] op_sel_hi:[1,1,0]
	v_fma_mix_f32 v191, v82, v64, v191 op_sel:[1,1,0] op_sel_hi:[1,1,0]
	v_fma_mix_f32 v192, v83, v64, v192 op_sel:[0,1,0] op_sel_hi:[1,1,0]
	v_fma_mix_f32 v193, v83, v64, v193 op_sel:[1,1,0] op_sel_hi:[1,1,0]
	v_fma_mix_f32 v194, v84, v64, v194 op_sel:[0,1,0] op_sel_hi:[1,1,0]
	v_fma_mix_f32 v195, v84, v64, v195 op_sel:[1,1,0] op_sel_hi:[1,1,0]
	v_fma_mix_f32 v196, v85, v64, v196 op_sel:[0,1,0] op_sel_hi:[1,1,0]
	v_fma_mix_f32 v197, v85, v64, v197 op_sel:[1,1,0] op_sel_hi:[1,1,0]
	v_fma_mix_f32 v190, v86, v65, v190 op_sel:[0,1,0] op_sel_hi:[1,1,0]
	v_fma_mix_f32 v191, v86, v65, v191 op_sel:[1,1,0] op_sel_hi:[1,1,0]
	v_fma_mix_f32 v192, v87, v65, v192 op_sel:[0,1,0] op_sel_hi:[1,1,0]
	v_fma_mix_f32 v193, v87, v65, v193 op_sel:[1,1,0] op_sel_hi:[1,1,0]
	v_fma_mix_f32 v194, v88, v65, v194 op_sel:[0,1,0] op_sel_hi:[1,1,0]
	v_fma_mix_f32 v195, v88, v65, v195 op_sel:[1,1,0] op_sel_hi:[1,1,0]
	v_fma_mix_f32 v196, v89, v65, v196 op_sel:[0,1,0] op_sel_hi:[1,1,0]
	v_fma_mix_f32 v197, v89, v65, v197 op_sel:[1,1,0] op_sel_hi:[1,1,0]
	s_addc_u32 s29, s56, s27
	global_load_dwordx4 v[62:65], v104, s[28:29]
	s_waitcnt vmcnt(2)
	s_add_u32 s28, s57, s26
	v_and_or_b32 v74, v66, v105, s19
	v_and_or_b32 v78, v67, v105, s19
	v_and_or_b32 v82, v68, v105, s19
	v_and_or_b32 v86, v69, v105, s19
	s_addc_u32 s29, s58, s27
	ds_read_b128 v[74:77], v74
	ds_read_b128 v[78:81], v78
	ds_read_b128 v[82:85], v82
	ds_read_b128 v[86:89], v86
	s_add_u32 s26, s59, s26
	s_waitcnt lgkmcnt(0)
	s_addc_u32 s27, s60, s27
	v_fma_mix_f32 v174, v74, v66, v174 op_sel:[0,1,0] op_sel_hi:[1,1,0]
	v_fma_mix_f32 v175, v74, v66, v175 op_sel:[1,1,0] op_sel_hi:[1,1,0]
	v_fma_mix_f32 v176, v75, v66, v176 op_sel:[0,1,0] op_sel_hi:[1,1,0]
	v_fma_mix_f32 v177, v75, v66, v177 op_sel:[1,1,0] op_sel_hi:[1,1,0]
	v_fma_mix_f32 v178, v76, v66, v178 op_sel:[0,1,0] op_sel_hi:[1,1,0]
	v_fma_mix_f32 v179, v76, v66, v179 op_sel:[1,1,0] op_sel_hi:[1,1,0]
	v_fma_mix_f32 v180, v77, v66, v180 op_sel:[0,1,0] op_sel_hi:[1,1,0]
	v_fma_mix_f32 v181, v77, v66, v181 op_sel:[1,1,0] op_sel_hi:[1,1,0]
	v_fma_mix_f32 v174, v78, v67, v174 op_sel:[0,1,0] op_sel_hi:[1,1,0]
	v_fma_mix_f32 v175, v78, v67, v175 op_sel:[1,1,0] op_sel_hi:[1,1,0]
	v_fma_mix_f32 v176, v79, v67, v176 op_sel:[0,1,0] op_sel_hi:[1,1,0]
	v_fma_mix_f32 v177, v79, v67, v177 op_sel:[1,1,0] op_sel_hi:[1,1,0]
	v_fma_mix_f32 v178, v80, v67, v178 op_sel:[0,1,0] op_sel_hi:[1,1,0]
	v_fma_mix_f32 v179, v80, v67, v179 op_sel:[1,1,0] op_sel_hi:[1,1,0]
	v_fma_mix_f32 v180, v81, v67, v180 op_sel:[0,1,0] op_sel_hi:[1,1,0]
	v_fma_mix_f32 v181, v81, v67, v181 op_sel:[1,1,0] op_sel_hi:[1,1,0]
	v_fma_mix_f32 v174, v82, v68, v174 op_sel:[0,1,0] op_sel_hi:[1,1,0]
	v_fma_mix_f32 v175, v82, v68, v175 op_sel:[1,1,0] op_sel_hi:[1,1,0]
	v_fma_mix_f32 v176, v83, v68, v176 op_sel:[0,1,0] op_sel_hi:[1,1,0]
	v_fma_mix_f32 v177, v83, v68, v177 op_sel:[1,1,0] op_sel_hi:[1,1,0]
	v_fma_mix_f32 v178, v84, v68, v178 op_sel:[0,1,0] op_sel_hi:[1,1,0]
	v_fma_mix_f32 v179, v84, v68, v179 op_sel:[1,1,0] op_sel_hi:[1,1,0]
	v_fma_mix_f32 v180, v85, v68, v180 op_sel:[0,1,0] op_sel_hi:[1,1,0]
	v_fma_mix_f32 v181, v85, v68, v181 op_sel:[1,1,0] op_sel_hi:[1,1,0]
	v_fma_mix_f32 v174, v86, v69, v174 op_sel:[0,1,0] op_sel_hi:[1,1,0]
	v_fma_mix_f32 v175, v86, v69, v175 op_sel:[1,1,0] op_sel_hi:[1,1,0]
	v_fma_mix_f32 v176, v87, v69, v176 op_sel:[0,1,0] op_sel_hi:[1,1,0]
	v_fma_mix_f32 v177, v87, v69, v177 op_sel:[1,1,0] op_sel_hi:[1,1,0]
	v_fma_mix_f32 v178, v88, v69, v178 op_sel:[0,1,0] op_sel_hi:[1,1,0]
	v_fma_mix_f32 v179, v88, v69, v179 op_sel:[1,1,0] op_sel_hi:[1,1,0]
	v_fma_mix_f32 v180, v89, v69, v180 op_sel:[0,1,0] op_sel_hi:[1,1,0]
	v_fma_mix_f32 v181, v89, v69, v181 op_sel:[1,1,0] op_sel_hi:[1,1,0]
	global_load_dwordx4 v[66:69], v104, s[28:29]
	s_waitcnt vmcnt(2)
	s_add_i32 s24, s24, 64
	v_and_or_b32 v74, v70, v105, s19
	v_and_or_b32 v78, v71, v105, s19
	v_and_or_b32 v82, v72, v105, s19
	v_and_or_b32 v86, v73, v105, s19
	s_cmp_lt_i32 s8, s39
	ds_read_b128 v[74:77], v74
	ds_read_b128 v[78:81], v78
	ds_read_b128 v[82:85], v82
	ds_read_b128 v[86:89], v86
	s_nop 0
	s_waitcnt lgkmcnt(0)
	s_nop 0
	v_fma_mix_f32 v166, v74, v70, v166 op_sel:[0,1,0] op_sel_hi:[1,1,0]
	v_fma_mix_f32 v167, v74, v70, v167 op_sel:[1,1,0] op_sel_hi:[1,1,0]
	v_fma_mix_f32 v168, v75, v70, v168 op_sel:[0,1,0] op_sel_hi:[1,1,0]
	v_fma_mix_f32 v169, v75, v70, v169 op_sel:[1,1,0] op_sel_hi:[1,1,0]
	v_fma_mix_f32 v170, v76, v70, v170 op_sel:[0,1,0] op_sel_hi:[1,1,0]
	v_fma_mix_f32 v171, v76, v70, v171 op_sel:[1,1,0] op_sel_hi:[1,1,0]
	v_fma_mix_f32 v172, v77, v70, v172 op_sel:[0,1,0] op_sel_hi:[1,1,0]
	v_fma_mix_f32 v173, v77, v70, v173 op_sel:[1,1,0] op_sel_hi:[1,1,0]
	v_fma_mix_f32 v166, v78, v71, v166 op_sel:[0,1,0] op_sel_hi:[1,1,0]
	v_fma_mix_f32 v167, v78, v71, v167 op_sel:[1,1,0] op_sel_hi:[1,1,0]
	v_fma_mix_f32 v168, v79, v71, v168 op_sel:[0,1,0] op_sel_hi:[1,1,0]
	v_fma_mix_f32 v169, v79, v71, v169 op_sel:[1,1,0] op_sel_hi:[1,1,0]
	v_fma_mix_f32 v170, v80, v71, v170 op_sel:[0,1,0] op_sel_hi:[1,1,0]
	v_fma_mix_f32 v171, v80, v71, v171 op_sel:[1,1,0] op_sel_hi:[1,1,0]
	v_fma_mix_f32 v172, v81, v71, v172 op_sel:[0,1,0] op_sel_hi:[1,1,0]
	v_fma_mix_f32 v173, v81, v71, v173 op_sel:[1,1,0] op_sel_hi:[1,1,0]
	v_fma_mix_f32 v166, v82, v72, v166 op_sel:[0,1,0] op_sel_hi:[1,1,0]
	v_fma_mix_f32 v167, v82, v72, v167 op_sel:[1,1,0] op_sel_hi:[1,1,0]
	v_fma_mix_f32 v168, v83, v72, v168 op_sel:[0,1,0] op_sel_hi:[1,1,0]
	v_fma_mix_f32 v169, v83, v72, v169 op_sel:[1,1,0] op_sel_hi:[1,1,0]
	v_fma_mix_f32 v170, v84, v72, v170 op_sel:[0,1,0] op_sel_hi:[1,1,0]
	v_fma_mix_f32 v171, v84, v72, v171 op_sel:[1,1,0] op_sel_hi:[1,1,0]
	v_fma_mix_f32 v172, v85, v72, v172 op_sel:[0,1,0] op_sel_hi:[1,1,0]
	v_fma_mix_f32 v173, v85, v72, v173 op_sel:[1,1,0] op_sel_hi:[1,1,0]
	v_fma_mix_f32 v166, v86, v73, v166 op_sel:[0,1,0] op_sel_hi:[1,1,0]
	v_fma_mix_f32 v167, v86, v73, v167 op_sel:[1,1,0] op_sel_hi:[1,1,0]
	v_fma_mix_f32 v168, v87, v73, v168 op_sel:[0,1,0] op_sel_hi:[1,1,0]
	v_fma_mix_f32 v169, v87, v73, v169 op_sel:[1,1,0] op_sel_hi:[1,1,0]
	v_fma_mix_f32 v170, v88, v73, v170 op_sel:[0,1,0] op_sel_hi:[1,1,0]
	v_fma_mix_f32 v171, v88, v73, v171 op_sel:[1,1,0] op_sel_hi:[1,1,0]
	v_fma_mix_f32 v172, v89, v73, v172 op_sel:[0,1,0] op_sel_hi:[1,1,0]
	v_fma_mix_f32 v173, v89, v73, v173 op_sel:[1,1,0] op_sel_hi:[1,1,0]
	global_load_dwordx4 v[70:73], v104, s[26:27]
	s_cbranch_scc1 .LBB3_43
	s_cmp_ge_i32 s8, s41
	s_cbranch_scc0 .LBB3_46
	s_branch .LBB3_48

.LBB3_47:
	s_waitcnt vmcnt(1)
	s_ashr_i32 s25, s24, 31
	v_and_or_b32 v74, v66, v105, s19
	v_and_or_b32 v78, v67, v105, s19
	v_and_or_b32 v82, v68, v105, s19
	v_and_or_b32 v86, v69, v105, s19
	s_add_i32 s8, s8, 1
	ds_read_b128 v[74:77], v74
	ds_read_b128 v[78:81], v78
	ds_read_b128 v[82:85], v82
	ds_read_b128 v[86:89], v86
	s_lshl_b64 s[26:27], s[24:25], 4
	s_waitcnt lgkmcnt(0)
	s_add_u32 s28, s57, s26
	v_fma_mix_f32 v174, v74, v66, v174 op_sel:[0,1,0] op_sel_hi:[1,1,0]
	v_fma_mix_f32 v175, v74, v66, v175 op_sel:[1,1,0] op_sel_hi:[1,1,0]
	v_fma_mix_f32 v176, v75, v66, v176 op_sel:[0,1,0] op_sel_hi:[1,1,0]
	v_fma_mix_f32 v177, v75, v66, v177 op_sel:[1,1,0] op_sel_hi:[1,1,0]
	v_fma_mix_f32 v178, v76, v66, v178 op_sel:[0,1,0] op_sel_hi:[1,1,0]
	v_fma_mix_f32 v179, v76, v66, v179 op_sel:[1,1,0] op_sel_hi:[1,1,0]
	v_fma_mix_f32 v180, v77, v66, v180 op_sel:[0,1,0] op_sel_hi:[1,1,0]
	v_fma_mix_f32 v181, v77, v66, v181 op_sel:[1,1,0] op_sel_hi:[1,1,0]
	v_fma_mix_f32 v174, v78, v67, v174 op_sel:[0,1,0] op_sel_hi:[1,1,0]
	v_fma_mix_f32 v175, v78, v67, v175 op_sel:[1,1,0] op_sel_hi:[1,1,0]
	v_fma_mix_f32 v176, v79, v67, v176 op_sel:[0,1,0] op_sel_hi:[1,1,0]
	v_fma_mix_f32 v177, v79, v67, v177 op_sel:[1,1,0] op_sel_hi:[1,1,0]
	v_fma_mix_f32 v178, v80, v67, v178 op_sel:[0,1,0] op_sel_hi:[1,1,0]
	v_fma_mix_f32 v179, v80, v67, v179 op_sel:[1,1,0] op_sel_hi:[1,1,0]
	v_fma_mix_f32 v180, v81, v67, v180 op_sel:[0,1,0] op_sel_hi:[1,1,0]
	v_fma_mix_f32 v181, v81, v67, v181 op_sel:[1,1,0] op_sel_hi:[1,1,0]
	v_fma_mix_f32 v174, v82, v68, v174 op_sel:[0,1,0] op_sel_hi:[1,1,0]
	v_fma_mix_f32 v175, v82, v68, v175 op_sel:[1,1,0] op_sel_hi:[1,1,0]
	v_fma_mix_f32 v176, v83, v68, v176 op_sel:[0,1,0] op_sel_hi:[1,1,0]
	v_fma_mix_f32 v177, v83, v68, v177 op_sel:[1,1,0] op_sel_hi:[1,1,0]
	v_fma_mix_f32 v178, v84, v68, v178 op_sel:[0,1,0] op_sel_hi:[1,1,0]
	v_fma_mix_f32 v179, v84, v68, v179 op_sel:[1,1,0] op_sel_hi:[1,1,0]
	v_fma_mix_f32 v180, v85, v68, v180 op_sel:[0,1,0] op_sel_hi:[1,1,0]
	v_fma_mix_f32 v181, v85, v68, v181 op_sel:[1,1,0] op_sel_hi:[1,1,0]
	v_fma_mix_f32 v174, v86, v69, v174 op_sel:[0,1,0] op_sel_hi:[1,1,0]
	v_fma_mix_f32 v175, v86, v69, v175 op_sel:[1,1,0] op_sel_hi:[1,1,0]
	v_fma_mix_f32 v176, v87, v69, v176 op_sel:[0,1,0] op_sel_hi:[1,1,0]
	v_fma_mix_f32 v177, v87, v69, v177 op_sel:[1,1,0] op_sel_hi:[1,1,0]
	v_fma_mix_f32 v178, v88, v69, v178 op_sel:[0,1,0] op_sel_hi:[1,1,0]
	v_fma_mix_f32 v179, v88, v69, v179 op_sel:[1,1,0] op_sel_hi:[1,1,0]
	v_fma_mix_f32 v180, v89, v69, v180 op_sel:[0,1,0] op_sel_hi:[1,1,0]
	v_fma_mix_f32 v181, v89, v69, v181 op_sel:[1,1,0] op_sel_hi:[1,1,0]
	s_addc_u32 s29, s58, s27
	global_load_dwordx4 v[66:69], v104, s[28:29]
	s_waitcnt vmcnt(1)
	s_add_u32 s26, s59, s26
	v_and_or_b32 v74, v70, v105, s19
	v_and_or_b32 v78, v71, v105, s19
	v_and_or_b32 v82, v72, v105, s19
	v_and_or_b32 v86, v73, v105, s19
	s_addc_u32 s27, s60, s27
	ds_read_b128 v[74:77], v74
	ds_read_b128 v[78:81], v78
	ds_read_b128 v[82:85], v82
	ds_read_b128 v[86:89], v86
	s_add_i32 s24, s24, 64
	s_waitcnt lgkmcnt(0)
	s_cmp_lt_i32 s8, s41
	v_fma_mix_f32 v166, v74, v70, v166 op_sel:[0,1,0] op_sel_hi:[1,1,0]
	v_fma_mix_f32 v167, v74, v70, v167 op_sel:[1,1,0] op_sel_hi:[1,1,0]
	v_fma_mix_f32 v168, v75, v70, v168 op_sel:[0,1,0] op_sel_hi:[1,1,0]
	v_fma_mix_f32 v169, v75, v70, v169 op_sel:[1,1,0] op_sel_hi:[1,1,0]
	v_fma_mix_f32 v170, v76, v70, v170 op_sel:[0,1,0] op_sel_hi:[1,1,0]
	v_fma_mix_f32 v171, v76, v70, v171 op_sel:[1,1,0] op_sel_hi:[1,1,0]
	v_fma_mix_f32 v172, v77, v70, v172 op_sel:[0,1,0] op_sel_hi:[1,1,0]
	v_fma_mix_f32 v173, v77, v70, v173 op_sel:[1,1,0] op_sel_hi:[1,1,0]
	v_fma_mix_f32 v166, v78, v71, v166 op_sel:[0,1,0] op_sel_hi:[1,1,0]
	v_fma_mix_f32 v167, v78, v71, v167 op_sel:[1,1,0] op_sel_hi:[1,1,0]
	v_fma_mix_f32 v168, v79, v71, v168 op_sel:[0,1,0] op_sel_hi:[1,1,0]
	v_fma_mix_f32 v169, v79, v71, v169 op_sel:[1,1,0] op_sel_hi:[1,1,0]
	v_fma_mix_f32 v170, v80, v71, v170 op_sel:[0,1,0] op_sel_hi:[1,1,0]
	v_fma_mix_f32 v171, v80, v71, v171 op_sel:[1,1,0] op_sel_hi:[1,1,0]
	v_fma_mix_f32 v172, v81, v71, v172 op_sel:[0,1,0] op_sel_hi:[1,1,0]
	v_fma_mix_f32 v173, v81, v71, v173 op_sel:[1,1,0] op_sel_hi:[1,1,0]
	v_fma_mix_f32 v166, v82, v72, v166 op_sel:[0,1,0] op_sel_hi:[1,1,0]
	v_fma_mix_f32 v167, v82, v72, v167 op_sel:[1,1,0] op_sel_hi:[1,1,0]
	v_fma_mix_f32 v168, v83, v72, v168 op_sel:[0,1,0] op_sel_hi:[1,1,0]
	v_fma_mix_f32 v169, v83, v72, v169 op_sel:[1,1,0] op_sel_hi:[1,1,0]
	v_fma_mix_f32 v170, v84, v72, v170 op_sel:[0,1,0] op_sel_hi:[1,1,0]
	v_fma_mix_f32 v171, v84, v72, v171 op_sel:[1,1,0] op_sel_hi:[1,1,0]
	v_fma_mix_f32 v172, v85, v72, v172 op_sel:[0,1,0] op_sel_hi:[1,1,0]
	v_fma_mix_f32 v173, v85, v72, v173 op_sel:[1,1,0] op_sel_hi:[1,1,0]
	v_fma_mix_f32 v166, v86, v73, v166 op_sel:[0,1,0] op_sel_hi:[1,1,0]
	v_fma_mix_f32 v167, v86, v73, v167 op_sel:[1,1,0] op_sel_hi:[1,1,0]
	v_fma_mix_f32 v168, v87, v73, v168 op_sel:[0,1,0] op_sel_hi:[1,1,0]
	v_fma_mix_f32 v169, v87, v73, v169 op_sel:[1,1,0] op_sel_hi:[1,1,0]
	v_fma_mix_f32 v170, v88, v73, v170 op_sel:[0,1,0] op_sel_hi:[1,1,0]
	v_fma_mix_f32 v171, v88, v73, v171 op_sel:[1,1,0] op_sel_hi:[1,1,0]
	v_fma_mix_f32 v172, v89, v73, v172 op_sel:[0,1,0] op_sel_hi:[1,1,0]
	v_fma_mix_f32 v173, v89, v73, v173 op_sel:[1,1,0] op_sel_hi:[1,1,0]
	global_load_dwordx4 v[70:73], v104, s[26:27]
	s_cbranch_scc1 .LBB3_47

.LBB3_50:
	s_waitcnt vmcnt(0)
	s_ashr_i32 s25, s24, 31
	v_and_or_b32 v74, v70, v105, s19
	v_and_or_b32 v78, v71, v105, s19
	v_and_or_b32 v82, v72, v105, s19
	v_and_or_b32 v86, v73, v105, s19
	s_add_i32 s8, s8, 1
	ds_read_b128 v[74:77], v74
	ds_read_b128 v[78:81], v78
	ds_read_b128 v[82:85], v82
	ds_read_b128 v[86:89], v86
	s_lshl_b64 s[26:27], s[24:25], 4
	s_waitcnt lgkmcnt(0)
	s_add_u32 s26, s59, s26
	v_fma_mix_f32 v166, v74, v70, v166 op_sel:[0,1,0] op_sel_hi:[1,1,0]
	v_fma_mix_f32 v167, v74, v70, v167 op_sel:[1,1,0] op_sel_hi:[1,1,0]
	v_fma_mix_f32 v168, v75, v70, v168 op_sel:[0,1,0] op_sel_hi:[1,1,0]
	v_fma_mix_f32 v169, v75, v70, v169 op_sel:[1,1,0] op_sel_hi:[1,1,0]
	v_fma_mix_f32 v170, v76, v70, v170 op_sel:[0,1,0] op_sel_hi:[1,1,0]
	v_fma_mix_f32 v171, v76, v70, v171 op_sel:[1,1,0] op_sel_hi:[1,1,0]
	v_fma_mix_f32 v172, v77, v70, v172 op_sel:[0,1,0] op_sel_hi:[1,1,0]
	v_fma_mix_f32 v173, v77, v70, v173 op_sel:[1,1,0] op_sel_hi:[1,1,0]
	v_fma_mix_f32 v166, v78, v71, v166 op_sel:[0,1,0] op_sel_hi:[1,1,0]
	v_fma_mix_f32 v167, v78, v71, v167 op_sel:[1,1,0] op_sel_hi:[1,1,0]
	v_fma_mix_f32 v168, v79, v71, v168 op_sel:[0,1,0] op_sel_hi:[1,1,0]
	v_fma_mix_f32 v169, v79, v71, v169 op_sel:[1,1,0] op_sel_hi:[1,1,0]
	v_fma_mix_f32 v170, v80, v71, v170 op_sel:[0,1,0] op_sel_hi:[1,1,0]
	v_fma_mix_f32 v171, v80, v71, v171 op_sel:[1,1,0] op_sel_hi:[1,1,0]
	v_fma_mix_f32 v172, v81, v71, v172 op_sel:[0,1,0] op_sel_hi:[1,1,0]
	v_fma_mix_f32 v173, v81, v71, v173 op_sel:[1,1,0] op_sel_hi:[1,1,0]
	s_addc_u32 s27, s60, s27
	s_add_i32 s24, s24, 64
	v_fma_mix_f32 v166, v82, v72, v166 op_sel:[0,1,0] op_sel_hi:[1,1,0]
	v_fma_mix_f32 v167, v82, v72, v167 op_sel:[1,1,0] op_sel_hi:[1,1,0]
	v_fma_mix_f32 v168, v83, v72, v168 op_sel:[0,1,0] op_sel_hi:[1,1,0]
	v_fma_mix_f32 v169, v83, v72, v169 op_sel:[1,1,0] op_sel_hi:[1,1,0]
	v_fma_mix_f32 v170, v84, v72, v170 op_sel:[0,1,0] op_sel_hi:[1,1,0]
	v_fma_mix_f32 v171, v84, v72, v171 op_sel:[1,1,0] op_sel_hi:[1,1,0]
	v_fma_mix_f32 v172, v85, v72, v172 op_sel:[0,1,0] op_sel_hi:[1,1,0]
	v_fma_mix_f32 v173, v85, v72, v173 op_sel:[1,1,0] op_sel_hi:[1,1,0]
	s_cmp_lt_i32 s8, s42
	v_fma_mix_f32 v166, v86, v73, v166 op_sel:[0,1,0] op_sel_hi:[1,1,0]
	v_fma_mix_f32 v167, v86, v73, v167 op_sel:[1,1,0] op_sel_hi:[1,1,0]
	v_fma_mix_f32 v168, v87, v73, v168 op_sel:[0,1,0] op_sel_hi:[1,1,0]
	v_fma_mix_f32 v169, v87, v73, v169 op_sel:[1,1,0] op_sel_hi:[1,1,0]
	v_fma_mix_f32 v170, v88, v73, v170 op_sel:[0,1,0] op_sel_hi:[1,1,0]
	v_fma_mix_f32 v171, v88, v73, v171 op_sel:[1,1,0] op_sel_hi:[1,1,0]
	v_fma_mix_f32 v172, v89, v73, v172 op_sel:[0,1,0] op_sel_hi:[1,1,0]
	v_fma_mix_f32 v173, v89, v73, v173 op_sel:[1,1,0] op_sel_hi:[1,1,0]
	global_load_dwordx4 v[70:73], v104, s[26:27]
	s_cbranch_scc1 .LBB3_50
